# MoE gate/up fp6 conversion: experts 0-1 stay in P0, experts 2-3 hosted in the dense FFN gate/up GEMM unit epilogues (one 32-load item per unit per wave, issued at epilogue start, converted at its end)
# baseline (speedup 1.0000x reference)
; template <int MODE>
; __device__ __forceinline__ void tr_matrix6(const float* W, int nb, int K, int N, unsigned char* WT, int drows, int rot, int gw, int NGW, int lane, float wscale) {
;     const int nbn = N / 32, per = (K / 256) * nbn, total = nb * per;
;     int it = gw - rot; if (it < 0) it += NGW;
;     const int c = lane & 7, q = lane >> 3;
;     for (; it < total; it += NGW) {
;         const int e = it / per, r = it - e * per, kb = r / nbn, nbk = r - kb * nbn, n0 = nbk * 32, k0 = kb * 256;
;         const float* src = W + (size_t)e * K * N + (size_t)(k0 + 32 * q) * N + n0 + 4 * c;
;         f32x4 v[32];
; #pragma unroll
;         for (int i = 0; i < 32; ++i) v[i] = *(const f32x4*)(src + (size_t)i * N);
.LBB0_56:
	s_mul_hi_i32 s6, s46, 0x92492493
	s_add_i32 s6, s6, s46
	s_lshr_b32 s7, s6, 31
	s_ashr_i32 s6, s6, 10
	s_add_i32 s6, s6, s7
	s_mul_i32 s7, s6, 0xfffff900
	s_mul_i32 s8, s6, 0x700
	s_mul_hi_i32 s9, s6, 0x3800000
	s_mul_i32 s10, s6, 0x3800000
	s_mul_hi_i32 s12, s6, 0x1c00000
	s_mul_i32 s13, s6, 0x1c00000
	s_add_i32 s6, s46, s7
	s_mul_hi_i32 s7, s6, 0x92492493
	s_add_i32 s7, s7, s6
	s_lshr_b32 s6, s7, 31
	s_ashr_i32 s7, s7, 7
	s_add_i32 s6, s7, s6
	s_mul_i32 s7, s6, 0xffffff20
	s_sub_i32 s7, s7, s8
	s_add_i32 s7, s46, s7
	s_lshl_b32 s6, s6, 8
	s_lshl_b32 s8, s7, 5
	s_add_u32 s10, s22, s10
	s_addc_u32 s11, s23, s9
	v_or_b32_e32 v4, s6, v146
	v_mov_b64_e32 v[2:3], s[10:11]
	s_ashr_i32 s9, s8, 31
	s_lshl_b32 s7, s7, 6
	v_mad_i64_i32 v[2:3], s[10:11], v4, s0, v[2:3]
	s_and_b32 s18, s8, 0x60
	s_and_b32 s7, s7, 0xffffff00
	v_lshl_add_u64 v[2:3], s[8:9], 2, v[2:3]
	s_add_u32 s10, s40, s13
	v_lshl_add_u64 v[8:9], v[2:3], 0, v[148:149]
	s_addc_u32 s11, s41, s12
	s_or_b32 s8, s7, s18
	v_add_co_u32_e32 v10, vcc, s0, v8
	v_or_b32_e32 v6, s8, v132
	s_nop 0
	v_addc_co_u32_e32 v11, vcc, 0, v9, vcc
	s_mov_b32 s8, 0xe000
	v_add_co_u32_e32 v12, vcc, s8, v8
	s_mov_b32 s8, 0x15000
	s_nop 0
	v_addc_co_u32_e32 v13, vcc, 0, v9, vcc
	v_add_co_u32_e32 v16, vcc, s8, v8
	s_mov_b32 s8, 0x1c000
	s_nop 0
	v_addc_co_u32_e32 v17, vcc, 0, v9, vcc
	v_add_co_u32_e32 v20, vcc, s8, v8
	s_mov_b32 s8, 0x23000
	s_nop 0
	v_addc_co_u32_e32 v21, vcc, 0, v9, vcc
	v_add_co_u32_e32 v24, vcc, s8, v8
	s_mov_b32 s8, 0x2a000
	s_nop 0
	v_addc_co_u32_e32 v25, vcc, 0, v9, vcc
	v_add_co_u32_e32 v28, vcc, s8, v8
	s_mov_b32 s8, 0x31000
	s_nop 0
	v_addc_co_u32_e32 v29, vcc, 0, v9, vcc
	v_add_co_u32_e32 v32, vcc, s8, v8
	s_mov_b32 s8, 0x38000
	s_nop 0
	v_addc_co_u32_e32 v33, vcc, 0, v9, vcc
	s_waitcnt vmcnt(15)
	v_add_co_u32_e32 v36, vcc, s8, v8
	s_mov_b32 s8, 0x3f000
	s_nop 0
	v_addc_co_u32_e32 v37, vcc, 0, v9, vcc
	s_waitcnt vmcnt(14)
	v_add_co_u32_e32 v40, vcc, s8, v8
	s_mov_b32 s8, 0x46000
	s_nop 0
	v_addc_co_u32_e32 v41, vcc, 0, v9, vcc
	s_waitcnt vmcnt(13)
	v_add_co_u32_e32 v44, vcc, s8, v8
	s_mov_b32 s8, 0x4d000
	s_nop 0
	v_addc_co_u32_e32 v45, vcc, 0, v9, vcc
	s_waitcnt vmcnt(12)
	v_add_co_u32_e32 v48, vcc, s8, v8
	s_mov_b32 s8, 0x54000
	s_nop 0
	v_addc_co_u32_e32 v49, vcc, 0, v9, vcc
	s_waitcnt vmcnt(7)
	v_add_co_u32_e32 v52, vcc, s8, v8
	s_mov_b32 s8, 0x5b000
	s_nop 0
	v_addc_co_u32_e32 v53, vcc, 0, v9, vcc
	s_waitcnt vmcnt(6)
	v_add_co_u32_e32 v56, vcc, s8, v8
	s_mov_b32 s8, 0x62000
	s_nop 0
	v_addc_co_u32_e32 v57, vcc, 0, v9, vcc
	s_waitcnt vmcnt(5)
	v_add_co_u32_e32 v60, vcc, s8, v8
	s_mov_b32 s8, 0x69000
	s_nop 0
	v_addc_co_u32_e32 v61, vcc, 0, v9, vcc
	s_waitcnt vmcnt(4)
	v_add_co_u32_e32 v64, vcc, s8, v8
	s_mov_b32 s8, 0x70000
	s_nop 0
	v_addc_co_u32_e32 v65, vcc, 0, v9, vcc
	v_add_co_u32_e32 v68, vcc, s8, v8
	s_mov_b32 s8, 0x77000
	s_nop 0
	v_addc_co_u32_e32 v69, vcc, 0, v9, vcc
	v_add_co_u32_e32 v72, vcc, s8, v8
	s_mov_b32 s8, 0x7e000
	s_nop 0
	v_addc_co_u32_e32 v73, vcc, 0, v9, vcc
	v_add_co_u32_e32 v76, vcc, s8, v8
	s_mov_b32 s8, 0x85000
	s_nop 0
	v_addc_co_u32_e32 v77, vcc, 0, v9, vcc
	v_add_co_u32_e32 v80, vcc, s8, v8
	s_mov_b32 s8, 0x8c000
	s_nop 0
	v_addc_co_u32_e32 v81, vcc, 0, v9, vcc
	v_add_co_u32_e32 v84, vcc, s8, v8
	global_load_dwordx4 v[2:5], v[8:9], off
	s_nop 0
	v_addc_co_u32_e32 v85, vcc, 0, v9, vcc
	v_add_co_u32_e32 v88, vcc, s1, v8
	v_ashrrev_i32_e32 v7, 31, v6
	s_nop 0
	v_addc_co_u32_e32 v89, vcc, 0, v9, vcc
	v_add_co_u32_e32 v92, vcc, s5, v8
	v_lshlrev_b64 v[6:7], 11, v[6:7]
	s_nop 0
	v_addc_co_u32_e32 v93, vcc, 0, v9, vcc
	v_add_co_u32_e32 v96, vcc, s14, v8
	s_ashr_i32 s7, s6, 31
	s_nop 0
	v_addc_co_u32_e32 v97, vcc, 0, v9, vcc
	v_add_co_u32_e32 v100, vcc, s15, v8
	v_lshl_add_u64 v[6:7], s[10:11], 0, v[6:7]
	s_nop 0
	v_addc_co_u32_e32 v101, vcc, 0, v9, vcc
	v_add_co_u32_e32 v104, vcc, s16, v8
	v_lshl_add_u64 v[6:7], v[6:7], 0, s[6:7]
	s_nop 0
	v_addc_co_u32_e32 v105, vcc, 0, v9, vcc
	v_add_co_u32_e32 v108, vcc, s17, v8
	v_lshl_add_u64 v[136:137], v[6:7], 0, v[146:147]
	s_nop 0
	v_addc_co_u32_e32 v109, vcc, 0, v9, vcc
	v_add_co_u32_e32 v112, vcc, s33, v8
	v_mov_b32_e32 v131, v130
	s_nop 0
	v_addc_co_u32_e32 v113, vcc, 0, v9, vcc
	v_add_co_u32_e32 v116, vcc, s38, v8
	s_add_i32 s46, s46, s72
	s_nop 0
	v_addc_co_u32_e32 v117, vcc, 0, v9, vcc
	v_add_co_u32_e32 v120, vcc, s39, v8
	s_cmpk_lt_i32 s46, 0xe00
	s_nop 0
	v_addc_co_u32_e32 v121, vcc, 0, v9, vcc
	v_add_co_u32_e32 v124, vcc, s42, v8
	s_nop 1
	v_addc_co_u32_e32 v125, vcc, 0, v9, vcc
	v_add_co_u32_e32 v128, vcc, s43, v8
	s_nop 1
	v_addc_co_u32_e32 v129, vcc, 0, v9, vcc
	global_load_dwordx4 v[8:11], v[10:11], off
	s_nop 0
	global_load_dwordx4 v[12:15], v[12:13], off
	s_nop 0
	global_load_dwordx4 v[16:19], v[16:17], off
	s_nop 0
	global_load_dwordx4 v[20:23], v[20:21], off
	s_nop 0
	global_load_dwordx4 v[24:27], v[24:25], off
	s_nop 0
	global_load_dwordx4 v[28:31], v[28:29], off
	s_nop 0
	global_load_dwordx4 v[32:35], v[32:33], off
	s_nop 0
	global_load_dwordx4 v[36:39], v[36:37], off
	s_nop 0
	global_load_dwordx4 v[40:43], v[40:41], off
	s_nop 0
	global_load_dwordx4 v[44:47], v[44:45], off
	s_nop 0
	global_load_dwordx4 v[48:51], v[48:49], off
	s_nop 0
	global_load_dwordx4 v[52:55], v[52:53], off
	s_nop 0
	global_load_dwordx4 v[56:59], v[56:57], off
	s_nop 0
	global_load_dwordx4 v[60:63], v[60:61], off
	s_nop 0
	global_load_dwordx4 v[64:67], v[64:65], off
	s_nop 0
	global_load_dwordx4 v[68:71], v[68:69], off
	s_nop 0
	global_load_dwordx4 v[72:75], v[72:73], off
	s_nop 0
	global_load_dwordx4 v[76:79], v[76:77], off
	s_nop 0
	global_load_dwordx4 v[80:83], v[80:81], off
	s_nop 0
	global_load_dwordx4 v[84:87], v[84:85], off
	s_nop 0
	global_load_dwordx4 v[88:91], v[88:89], off
	s_nop 0
	global_load_dwordx4 v[92:95], v[92:93], off
	s_nop 0
	global_load_dwordx4 v[96:99], v[96:97], off
	s_nop 0
	global_load_dwordx4 v[100:103], v[100:101], off
	s_nop 0
	global_load_dwordx4 v[104:107], v[104:105], off
	s_nop 0
	global_load_dwordx4 v[108:111], v[108:109], off
	s_nop 0
	global_load_dwordx4 v[112:115], v[112:113], off
	s_nop 0
	global_load_dwordx4 v[116:119], v[116:117], off
	s_nop 0
	global_load_dwordx4 v[120:123], v[120:121], off
	s_nop 0
	global_load_dwordx4 v[124:127], v[124:125], off
	s_nop 0
	global_load_dwordx4 v[138:141], v[128:129], off
	s_waitcnt vmcnt(31)
; template <int MODE>
; __device__ __forceinline__ void tr_matrix6(const float* W, int nb, int K, int N, unsigned char* WT, int drows, int rot, int gw, int NGW, int lane, float wscale) {
;     ...
;         for (int j = 0; j < 4; ++j) { float x[32];
; #pragma unroll
;             for (int i = 0; i < 32; ++i) x[i] = v[i][j] * wscale;
	v_mul_f32_e32 v2, 0x42b40000, v2
	v_mul_f32_e32 v3, 0x42b40000, v3
	v_mul_f32_e32 v4, 0x42b40000, v4
	v_mul_f32_e32 v5, 0x42b40000, v5
	v_med3_f32 v2, v2, s44, v133
	v_add_co_u32_e32 v134, vcc, s45, v136
	s_waitcnt vmcnt(30)
	v_mul_f32_e32 v6, 0x42b40000, v8
	v_mul_f32_e32 v128, 0x42b40000, v9
	v_mul_f32_e32 v129, 0x42b40000, v10
	v_mul_f32_e32 v142, 0x42b40000, v11
	s_waitcnt vmcnt(29)
	v_mul_f32_e32 v7, 0x42b40000, v12
	v_mul_f32_e32 v143, 0x42b40000, v13
	v_mul_f32_e32 v145, 0x42b40000, v14
	v_mul_f32_e32 v150, 0x42b40000, v15
	s_waitcnt vmcnt(28)
	v_mul_f32_e32 v8, 0x42b40000, v16
	v_mul_f32_e32 v151, 0x42b40000, v17
	s_waitcnt vmcnt(27)
	v_mul_f32_e32 v9, 0x42b40000, v20
	v_mul_f32_e32 v20, 0x42b40000, v22
	v_mul_f32_e32 v22, 0x42b40000, v23
	s_waitcnt vmcnt(26)
	v_mul_f32_e32 v10, 0x42b40000, v24
	v_mul_f32_e32 v23, 0x42b40000, v26
	v_mul_f32_e32 v24, 0x42b40000, v27
	s_waitcnt vmcnt(25)
	v_mul_f32_e32 v11, 0x42b40000, v28
	v_mul_f32_e32 v26, 0x42b40000, v30
	v_mul_f32_e32 v27, 0x42b40000, v31
	s_waitcnt vmcnt(24)
	v_mul_f32_e32 v12, 0x42b40000, v32
	v_mul_f32_e32 v28, 0x42b40000, v33
	v_mul_f32_e32 v30, 0x42b40000, v35
	s_waitcnt vmcnt(23)
	v_mul_f32_e32 v13, 0x42b40000, v36
	v_mul_f32_e32 v31, 0x42b40000, v37
	v_mul_f32_e32 v32, 0x42b40000, v38
	v_mul_f32_e32 v33, 0x42b40000, v39
	s_waitcnt vmcnt(22)
	v_mul_f32_e32 v14, 0x42b40000, v40
	v_mul_f32_e32 v35, 0x42b40000, v41
	v_mul_f32_e32 v155, 0x42b40000, v42
	v_mul_f32_e32 v156, 0x42b40000, v43
	s_waitcnt vmcnt(21)
	v_mul_f32_e32 v15, 0x42b40000, v44
	v_mul_f32_e32 v157, 0x42b40000, v47
	s_waitcnt vmcnt(20)
	v_mul_f32_e32 v16, 0x42b40000, v48
	v_mul_f32_e32 v37, 0x42b40000, v49
	v_mul_f32_e32 v158, 0x42b40000, v51
	s_waitcnt vmcnt(19)
	v_mul_f32_e32 v17, 0x42b40000, v52
	v_mul_f32_e32 v38, 0x42b40000, v53
	v_mul_f32_e32 v159, 0x42b40000, v55
	s_waitcnt vmcnt(18)
	v_mul_f32_e32 v39, 0x42b40000, v56
	v_mul_f32_e32 v40, 0x42b40000, v57
	v_mul_f32_e32 v47, 0x42b40000, v58
	v_mul_f32_e32 v160, 0x42b40000, v59
	s_waitcnt vmcnt(17)
	v_mul_f32_e32 v41, 0x42b40000, v60
	v_mul_f32_e32 v42, 0x42b40000, v61
	v_mul_f32_e32 v161, 0x42b40000, v63
	s_waitcnt vmcnt(16)
	v_mul_f32_e32 v43, 0x42b40000, v64
	v_mul_f32_e32 v49, 0x42b40000, v65
	s_waitcnt vmcnt(15)
	v_mul_f32_e32 v51, 0x42b40000, v68
	s_waitcnt vmcnt(14)
	v_mul_f32_e32 v53, 0x42b40000, v72
	v_mul_f32_e32 v166, 0x42b40000, v74
	v_mul_f32_e32 v167, 0x42b40000, v75
	s_waitcnt vmcnt(13)
	v_mul_f32_e32 v55, 0x42b40000, v76
	v_mul_f32_e32 v56, 0x42b40000, v77
	v_mul_f32_e32 v168, 0x42b40000, v78
	v_mul_f32_e32 v169, 0x42b40000, v79
	s_waitcnt vmcnt(12)
	v_mul_f32_e32 v57, 0x42b40000, v80
	v_mul_f32_e32 v58, 0x42b40000, v81
	s_waitcnt vmcnt(11)
	v_mul_f32_e32 v59, 0x42b40000, v84
	s_waitcnt vmcnt(10)
	v_mul_f32_e32 v61, 0x42b40000, v88
	s_waitcnt vmcnt(9)
	v_mul_f32_e32 v63, 0x42b40000, v92
	s_waitcnt vmcnt(8)
	v_mul_f32_e32 v65, 0x42b40000, v96
	s_waitcnt vmcnt(7)
	v_mul_f32_e32 v74, 0x42b40000, v100
	s_waitcnt vmcnt(6)
	v_mul_f32_e32 v75, 0x42b40000, v104
	s_waitcnt vmcnt(5)
	v_mul_f32_e32 v76, 0x42b40000, v108
	s_waitcnt vmcnt(4)
	v_mul_f32_e32 v77, 0x42b40000, v112
	s_waitcnt vmcnt(3)
	v_mul_f32_e32 v78, 0x42b40000, v116
	s_waitcnt vmcnt(2)
	v_mul_f32_e32 v79, 0x42b40000, v120
	s_waitcnt vmcnt(1)
	v_mul_f32_e32 v80, 0x42b40000, v124
	s_waitcnt vmcnt(0)
	v_mul_f32_e32 v81, 0x42b40000, v138
	v_mul_f32_e32 v152, 0x42b40000, v18
	v_mul_f32_e32 v153, 0x42b40000, v19
	v_mul_f32_e32 v19, 0x42b40000, v21
	v_mul_f32_e32 v21, 0x42b40000, v25
	v_mul_f32_e32 v25, 0x42b40000, v29
	v_mul_f32_e32 v29, 0x42b40000, v34
	v_mul_f32_e32 v36, 0x42b40000, v45
	v_mul_f32_e32 v44, 0x42b40000, v46
	v_mul_f32_e32 v45, 0x42b40000, v50
	v_mul_f32_e32 v46, 0x42b40000, v54
	v_mul_f32_e32 v48, 0x42b40000, v62
	v_mul_f32_e32 v162, 0x42b40000, v66
	v_mul_f32_e32 v163, 0x42b40000, v67
	v_mul_f32_e32 v52, 0x42b40000, v69
	v_mul_f32_e32 v164, 0x42b40000, v70
	v_mul_f32_e32 v165, 0x42b40000, v71
	v_mul_f32_e32 v54, 0x42b40000, v73
	v_mul_f32_e32 v171, 0x42b40000, v83
	v_mul_f32_e32 v60, 0x42b40000, v85
	v_mul_f32_e32 v173, 0x42b40000, v87
	v_mul_f32_e32 v62, 0x42b40000, v89
	v_mul_f32_e32 v174, 0x42b40000, v90
	v_mul_f32_e32 v175, 0x42b40000, v91
	v_mul_f32_e32 v64, 0x42b40000, v93
	v_mul_f32_e32 v176, 0x42b40000, v94
	v_mul_f32_e32 v177, 0x42b40000, v95
	v_mul_f32_e32 v89, 0x42b40000, v97
	v_mul_f32_e32 v179, 0x42b40000, v99
	v_mul_f32_e32 v90, 0x42b40000, v101
	v_mul_f32_e32 v181, 0x42b40000, v103
	v_mul_f32_e32 v91, 0x42b40000, v105
	v_mul_f32_e32 v183, 0x42b40000, v107
	v_mul_f32_e32 v92, 0x42b40000, v109
	v_mul_f32_e32 v184, 0x42b40000, v111
	v_mul_f32_e32 v93, 0x42b40000, v113
	v_mul_f32_e32 v185, 0x42b40000, v115
	v_mul_f32_e32 v94, 0x42b40000, v117
	v_mul_f32_e32 v186, 0x42b40000, v119
	v_mul_f32_e32 v95, 0x42b40000, v121
	v_mul_f32_e32 v187, 0x42b40000, v123
	v_mul_f32_e32 v96, 0x42b40000, v125
	v_mul_f32_e32 v188, 0x42b40000, v127
	v_mul_f32_e32 v97, 0x42b40000, v139
	v_mul_f32_e32 v138, 0x42b40000, v141
	v_med3_f32 v50, v3, s44, v133
	v_med3_f32 v34, v4, s44, v133
	v_med3_f32 v18, v5, s44, v133
	v_med3_f32 v3, v6, s44, v133
	v_med3_f32 v66, v51, s44, v133
	v_med3_f32 v67, v53, s44, v133
	v_med3_f32 v4, v7, s44, v133
	v_med3_f32 v68, v55, s44, v133
	v_med3_f32 v5, v8, s44, v133
	v_med3_f32 v69, v57, s44, v133
	v_med3_f32 v6, v9, s44, v133
	v_med3_f32 v70, v59, s44, v133
	v_med3_f32 v7, v10, s44, v133
	v_med3_f32 v71, v61, s44, v133
	v_med3_f32 v8, v11, s44, v133
	v_med3_f32 v72, v63, s44, v133
	v_med3_f32 v9, v12, s44, v133
	v_med3_f32 v73, v65, s44, v133
	v_med3_f32 v10, v13, s44, v133
	v_med3_f32 v74, v74, s44, v133
	v_med3_f32 v11, v14, s44, v133
; template <int MODE>
; __device__ __forceinline__ void tr_matrix6(const float* W, int nb, int K, int N, unsigned char* WT, int drows, int rot, int gw, int NGW, int lane, float wscale) {
;     ...
;         for (int j = 0; j < 4; ++j) { float x[32];
; #pragma unroll
;             for (int i = 0; i < 32; ++i) x[i] = v[i][j] * wscale;
;             const v6u w = pk32_fp6(x);
;             *(u32x4*)(dst + (size_t)j * K) = (u32x4){w[0], w[1], w[2], w[3]}; *(u32x4*)(dst + (size_t)j * K + 16) = (u32x4){w[4], w[5], 0u, 0u}; }
	v_med3_f32 v75, v75, s44, v133
	v_med3_f32 v12, v15, s44, v133
	v_med3_f32 v76, v76, s44, v133
	v_med3_f32 v13, v16, s44, v133
	v_med3_f32 v77, v77, s44, v133
	v_med3_f32 v14, v17, s44, v133
	v_med3_f32 v78, v78, s44, v133
	v_med3_f32 v15, v39, s44, v133
	v_med3_f32 v79, v79, s44, v133
	v_med3_f32 v16, v41, s44, v133
	v_med3_f32 v80, v80, s44, v133
	v_med3_f32 v17, v43, s44, v133
	v_med3_f32 v81, v81, s44, v133
	v_mul_f32_e32 v170, 0x42b40000, v82
	v_mul_f32_e32 v172, 0x42b40000, v86
	v_mul_f32_e32 v178, 0x42b40000, v98
	v_mul_f32_e32 v180, 0x42b40000, v102
	v_mul_f32_e32 v182, 0x42b40000, v106
	v_mul_f32_e32 v108, 0x42b40000, v110
	v_mul_f32_e32 v109, 0x42b40000, v114
	v_mul_f32_e32 v110, 0x42b40000, v118
	v_mul_f32_e32 v111, 0x42b40000, v122
	v_mul_f32_e32 v112, 0x42b40000, v126
	v_mul_f32_e32 v113, 0x42b40000, v140
	v_med3_f32 v51, v128, s44, v133
	v_med3_f32 v82, v52, s44, v133
	v_med3_f32 v83, v54, s44, v133
	v_med3_f32 v52, v143, s44, v133
	v_med3_f32 v84, v56, s44, v133
	v_med3_f32 v53, v151, s44, v133
	v_med3_f32 v85, v58, s44, v133
	v_med3_f32 v54, v19, s44, v133
	v_med3_f32 v86, v60, s44, v133
	v_med3_f32 v55, v21, s44, v133
	v_med3_f32 v87, v62, s44, v133
	v_med3_f32 v56, v25, s44, v133
	v_med3_f32 v88, v64, s44, v133
	v_med3_f32 v57, v28, s44, v133
	v_med3_f32 v89, v89, s44, v133
	v_med3_f32 v58, v31, s44, v133
	v_med3_f32 v90, v90, s44, v133
	v_med3_f32 v59, v35, s44, v133
	v_med3_f32 v91, v91, s44, v133
	v_med3_f32 v60, v36, s44, v133
	v_med3_f32 v92, v92, s44, v133
	v_med3_f32 v61, v37, s44, v133
	v_med3_f32 v93, v93, s44, v133
	v_med3_f32 v62, v38, s44, v133
	v_med3_f32 v94, v94, s44, v133
	v_med3_f32 v63, v40, s44, v133
	v_med3_f32 v95, v95, s44, v133
	v_med3_f32 v64, v42, s44, v133
	v_med3_f32 v96, v96, s44, v133
	v_med3_f32 v65, v49, s44, v133
	v_med3_f32 v97, v97, s44, v133
	v_med3_f32 v35, v129, s44, v133
	v_med3_f32 v38, v20, s44, v133
	v_med3_f32 v39, v23, s44, v133
	v_med3_f32 v40, v26, s44, v133
	v_med3_f32 v41, v29, s44, v133
	v_med3_f32 v42, v32, s44, v133
	v_med3_f32 v19, v142, s44, v133
	v_med3_f32 v114, v165, s44, v133
	v_med3_f32 v115, v167, s44, v133
	v_med3_f32 v20, v150, s44, v133
	v_med3_f32 v116, v169, s44, v133
	v_med3_f32 v21, v153, s44, v133
	v_med3_f32 v117, v171, s44, v133
	v_med3_f32 v22, v22, s44, v133
	v_med3_f32 v118, v173, s44, v133
	v_med3_f32 v23, v24, s44, v133
	v_med3_f32 v119, v175, s44, v133
	v_med3_f32 v24, v27, s44, v133
	v_med3_f32 v120, v177, s44, v133
	v_med3_f32 v25, v30, s44, v133
	v_med3_f32 v121, v179, s44, v133
	v_med3_f32 v26, v33, s44, v133
	v_med3_f32 v122, v181, s44, v133
	v_med3_f32 v27, v156, s44, v133
	v_med3_f32 v123, v183, s44, v133
	v_med3_f32 v28, v157, s44, v133
	v_med3_f32 v124, v184, s44, v133
	v_med3_f32 v29, v158, s44, v133
	v_med3_f32 v125, v185, s44, v133
	v_med3_f32 v30, v159, s44, v133
	v_med3_f32 v126, v186, s44, v133
	v_med3_f32 v31, v160, s44, v133
	v_med3_f32 v127, v187, s44, v133
	v_med3_f32 v32, v161, s44, v133
	v_med3_f32 v128, v188, s44, v133
	v_med3_f32 v33, v163, s44, v133
	v_med3_f32 v129, v138, s44, v133
	v_cvt_scalef32_2xpk16_fp6_f32 v[2:7], v[2:17], v[66:81], 1.0
	v_med3_f32 v98, v164, s44, v133
	v_med3_f32 v99, v166, s44, v133
	v_med3_f32 v36, v145, s44, v133
	v_med3_f32 v100, v168, s44, v133
	v_med3_f32 v37, v152, s44, v133
	v_med3_f32 v101, v170, s44, v133
	v_med3_f32 v102, v172, s44, v133
	v_med3_f32 v103, v174, s44, v133
	v_med3_f32 v104, v176, s44, v133
	v_med3_f32 v105, v178, s44, v133
	v_med3_f32 v106, v180, s44, v133
	v_med3_f32 v43, v155, s44, v133
	v_med3_f32 v107, v182, s44, v133
	v_med3_f32 v44, v44, s44, v133
	v_med3_f32 v108, v108, s44, v133
	v_med3_f32 v45, v45, s44, v133
	v_med3_f32 v109, v109, s44, v133
	v_med3_f32 v46, v46, s44, v133
	v_med3_f32 v110, v110, s44, v133
	v_med3_f32 v47, v47, s44, v133
	v_med3_f32 v111, v111, s44, v133
	v_med3_f32 v48, v48, s44, v133
	v_med3_f32 v112, v112, s44, v133
	v_med3_f32 v49, v162, s44, v133
	v_med3_f32 v113, v113, s44, v133
	v_cvt_scalef32_2xpk16_fp6_f32 v[8:13], v[50:65], v[82:97], 1.0
	v_cvt_scalef32_2xpk16_fp6_f32 v[14:19], v[18:33], v[114:129], 1.0
	v_mov_b32_e32 v128, v6
	v_mov_b32_e32 v129, v7
	v_addc_co_u32_e32 v135, vcc, 0, v137, vcc
	v_cvt_scalef32_2xpk16_fp6_f32 v[34:39], v[34:49], v[98:113], 1.0
	global_store_dwordx4 v[136:137], v[2:5], off
	global_store_dwordx4 v[136:137], v[8:11], off offset:2048
	global_store_dwordx4 v[134:135], v[34:37], off
	global_store_dwordx4 v[134:135], v[14:17], off offset:2048
	global_store_dwordx4 v[136:137], v[128:131], off offset:16
	s_nop 1
	v_mov_b32_e32 v128, v12
	v_mov_b32_e32 v129, v13
	global_store_dwordx4 v[136:137], v[128:131], off offset:2064
	s_nop 1
	v_mov_b32_e32 v128, v38
	v_mov_b32_e32 v129, v39
	global_store_dwordx4 v[134:135], v[128:131], off offset:16
	s_nop 1
	v_mov_b32_e32 v128, v18
	v_mov_b32_e32 v129, v19
	global_store_dwordx4 v[134:135], v[128:131], off offset:2064
	s_cbranch_scc1 .LBB0_56
	v_or_b32_e32 v145, 0x80, v132
	s_movk_i32 s0, 0x7000
	v_mov_b32_e32 v149, 0
	s_mov_b32 s1, 0x7e000
	s_mov_b32 s5, 0x85000
	s_mov_b32 s14, 0x8c000
	s_mov_b32 s15, 0x93000
	s_mov_b32 s16, 0x9a000
	s_mov_b32 s17, 0xa1000
	s_mov_b32 s22, 0xa8000
	s_mov_b32 s23, 0xaf000
	s_mov_b32 s33, 0xb6000
	s_mov_b32 s38, 0xbd000
	s_mov_b32 s39, 0xc4000
	s_mov_b32 s42, 0xcb000
	s_mov_b32 s43, 0xd2000
	s_mov_b32 s44, 0xd9000
	s_mov_b32 s45, 0xc0f00000
	s_movk_i32 s46, 0x1000
	v_mov_b32_e32 v155, 0x40f00000
; template <int MODE>
; __device__ __forceinline__ void tr_matrix6(const float* W, int nb, int K, int N, unsigned char* WT, int drows, int rot, int gw, int NGW, int lane, float wscale) {
;     const int nbn = N / 32, per = (K / 256) * nbn, total = nb * per;
;     int it = gw - rot; if (it < 0) it += NGW;
;     const int c = lane & 7, q = lane >> 3;
;     for (; it < total; it += NGW) {
;         const int e = it / per, r = it - e * per, kb = r / nbn, nbk = r - kb * nbn, n0 = nbk * 32, k0 = kb * 256;
;         const float* src = W + (size_t)e * K * N + (size_t)(k0 + 32 * q) * N + n0 + 4 * c;
;         f32x4 v[32];
; #pragma unroll
;         for (int i = 0; i < 32; ++i) v[i] = *(const f32x4*)(src + (size_t)i * N);
;         const int drow0 = (MODE == 0) ? n0 : ((n0 >> 7) * 256 + (n0 & 127) + (MODE == 2 ? 128 : 0));
;         unsigned char* dst = WT + (size_t)e * drows * K + (size_t)(drow0 + 4 * c) * K + k0 + 32 * q;
.LBB0_58:
	s_mul_hi_i32 s6, s3, 0x92492493
	s_add_i32 s6, s6, s3
	s_lshr_b32 s7, s6, 31
	s_ashr_i32 s6, s6, 10
	s_add_i32 s6, s6, s7
	s_mul_i32 s7, s6, 0xfffff900
	s_mul_i32 s8, s6, 0x700
	s_mul_hi_i32 s9, s6, 0x3800000
	s_mul_i32 s10, s6, 0x3800000
	s_mul_hi_i32 s12, s6, 0x1c00000
	s_mul_i32 s13, s6, 0x1c00000
	s_add_i32 s6, s3, s7
	s_mul_hi_i32 s7, s6, 0x92492493
	s_add_i32 s7, s7, s6
	s_lshr_b32 s6, s7, 31
	s_ashr_i32 s7, s7, 7
	s_add_i32 s6, s7, s6
	s_mul_i32 s7, s6, 0xffffff20
	s_sub_i32 s7, s7, s8
	s_add_i32 s7, s3, s7
	s_lshl_b32 s6, s6, 8
	s_lshl_b32 s8, s7, 5
	s_add_u32 s10, s24, s10
	s_addc_u32 s11, s25, s9
	v_or_b32_e32 v4, s6, v146
	v_mov_b64_e32 v[2:3], s[10:11]
	s_ashr_i32 s9, s8, 31
	s_lshl_b32 s7, s7, 6
	v_mad_i64_i32 v[2:3], s[10:11], v4, s0, v[2:3]
	s_and_b32 s18, s8, 0x60
	s_and_b32 s7, s7, 0xffffff00
	v_lshl_add_u64 v[2:3], s[8:9], 2, v[2:3]
	s_add_u32 s10, s40, s13
	v_lshl_add_u64 v[8:9], v[2:3], 0, v[148:149]
	s_addc_u32 s11, s41, s12
	s_or_b32 s8, s7, s18
	v_add_co_u32_e32 v10, vcc, s0, v8
	v_or_b32_e32 v6, s8, v145
	s_nop 0
	v_addc_co_u32_e32 v11, vcc, 0, v9, vcc
	s_mov_b32 s8, 0xe000
	v_add_co_u32_e32 v12, vcc, s8, v8
	s_mov_b32 s8, 0x15000
	s_nop 0
	v_addc_co_u32_e32 v13, vcc, 0, v9, vcc
	v_add_co_u32_e32 v16, vcc, s8, v8
	s_mov_b32 s8, 0x1c000
	s_nop 0
	v_addc_co_u32_e32 v17, vcc, 0, v9, vcc
	v_add_co_u32_e32 v20, vcc, s8, v8
	s_mov_b32 s8, 0x23000
	s_nop 0
	v_addc_co_u32_e32 v21, vcc, 0, v9, vcc
	v_add_co_u32_e32 v24, vcc, s8, v8
	s_mov_b32 s8, 0x2a000
	s_nop 0
	v_addc_co_u32_e32 v25, vcc, 0, v9, vcc
	v_add_co_u32_e32 v28, vcc, s8, v8
	s_mov_b32 s8, 0x31000
	s_nop 0
	v_addc_co_u32_e32 v29, vcc, 0, v9, vcc
	v_add_co_u32_e32 v32, vcc, s8, v8
	s_mov_b32 s8, 0x38000
	s_nop 0
	v_addc_co_u32_e32 v33, vcc, 0, v9, vcc
	v_add_co_u32_e32 v36, vcc, s8, v8
	s_mov_b32 s8, 0x3f000
	s_nop 0
	v_addc_co_u32_e32 v37, vcc, 0, v9, vcc
	v_add_co_u32_e32 v40, vcc, s8, v8
	s_mov_b32 s8, 0x46000
	s_nop 0
	v_addc_co_u32_e32 v41, vcc, 0, v9, vcc
	v_add_co_u32_e32 v44, vcc, s8, v8
	s_mov_b32 s8, 0x4d000
	s_nop 0
	v_addc_co_u32_e32 v45, vcc, 0, v9, vcc
	v_add_co_u32_e32 v48, vcc, s8, v8
	s_mov_b32 s8, 0x54000
	s_nop 0
	v_addc_co_u32_e32 v49, vcc, 0, v9, vcc
	v_add_co_u32_e32 v52, vcc, s8, v8
	s_mov_b32 s8, 0x5b000
	s_nop 0
	v_addc_co_u32_e32 v53, vcc, 0, v9, vcc
	v_add_co_u32_e32 v56, vcc, s8, v8
	s_mov_b32 s8, 0x62000
	s_nop 0
	v_addc_co_u32_e32 v57, vcc, 0, v9, vcc
	v_add_co_u32_e32 v60, vcc, s8, v8
	s_mov_b32 s8, 0x69000
	s_nop 0
	v_addc_co_u32_e32 v61, vcc, 0, v9, vcc
	v_add_co_u32_e32 v64, vcc, s8, v8
	s_mov_b32 s8, 0x70000
	s_nop 0
	v_addc_co_u32_e32 v65, vcc, 0, v9, vcc
	v_add_co_u32_e32 v68, vcc, s8, v8
	s_mov_b32 s8, 0x77000
	s_nop 0
	v_addc_co_u32_e32 v69, vcc, 0, v9, vcc
	v_add_co_u32_e32 v72, vcc, s8, v8
	global_load_dwordx4 v[2:5], v[8:9], off
	s_nop 0
	v_addc_co_u32_e32 v73, vcc, 0, v9, vcc
	v_add_co_u32_e32 v76, vcc, s1, v8
	v_ashrrev_i32_e32 v7, 31, v6
	s_nop 0
	v_addc_co_u32_e32 v77, vcc, 0, v9, vcc
	v_add_co_u32_e32 v80, vcc, s5, v8
	v_lshlrev_b64 v[6:7], 11, v[6:7]
	s_nop 0
	v_addc_co_u32_e32 v81, vcc, 0, v9, vcc
	v_add_co_u32_e32 v84, vcc, s14, v8
	s_ashr_i32 s7, s6, 31
	s_nop 0
	v_addc_co_u32_e32 v85, vcc, 0, v9, vcc
	v_add_co_u32_e32 v88, vcc, s15, v8
	v_lshl_add_u64 v[6:7], s[10:11], 0, v[6:7]
	s_nop 0
	v_addc_co_u32_e32 v89, vcc, 0, v9, vcc
	v_add_co_u32_e32 v92, vcc, s16, v8
	v_lshl_add_u64 v[6:7], v[6:7], 0, s[6:7]
	s_nop 0
	v_addc_co_u32_e32 v93, vcc, 0, v9, vcc
	v_add_co_u32_e32 v96, vcc, s17, v8
	v_lshl_add_u64 v[150:151], v[6:7], 0, v[146:147]
	s_nop 0
	v_addc_co_u32_e32 v97, vcc, 0, v9, vcc
	v_add_co_u32_e32 v100, vcc, s22, v8
	s_add_i32 s3, s3, s72
	s_nop 0
	v_addc_co_u32_e32 v101, vcc, 0, v9, vcc
	v_add_co_u32_e32 v104, vcc, s23, v8
	v_mov_b32_e32 v130, v149
	s_nop 0
	v_addc_co_u32_e32 v105, vcc, 0, v9, vcc
	v_add_co_u32_e32 v108, vcc, s33, v8
	v_mov_b32_e32 v131, v149
	s_nop 0
	v_addc_co_u32_e32 v109, vcc, 0, v9, vcc
	v_add_co_u32_e32 v112, vcc, s38, v8
	s_cmpk_lt_i32 s3, 0xe00
	s_nop 0
	v_addc_co_u32_e32 v113, vcc, 0, v9, vcc
	v_add_co_u32_e32 v116, vcc, s39, v8
	v_mov_b32_e32 v134, v149
	s_nop 0
	v_addc_co_u32_e32 v117, vcc, 0, v9, vcc
	v_add_co_u32_e32 v120, vcc, s42, v8
	v_mov_b32_e32 v135, v149
	s_nop 0
	v_addc_co_u32_e32 v121, vcc, 0, v9, vcc
	v_add_co_u32_e32 v124, vcc, s43, v8
	v_mov_b32_e32 v138, v149
	s_nop 0
	v_addc_co_u32_e32 v125, vcc, 0, v9, vcc
	v_add_co_u32_e32 v128, vcc, s44, v8
	v_mov_b32_e32 v139, v149
	s_nop 0
	v_addc_co_u32_e32 v129, vcc, 0, v9, vcc
	global_load_dwordx4 v[8:11], v[10:11], off
	s_nop 0
	global_load_dwordx4 v[12:15], v[12:13], off
	s_nop 0
	global_load_dwordx4 v[16:19], v[16:17], off
	s_nop 0
	global_load_dwordx4 v[20:23], v[20:21], off
	s_nop 0
	global_load_dwordx4 v[24:27], v[24:25], off
	s_nop 0
	global_load_dwordx4 v[28:31], v[28:29], off
	s_nop 0
	global_load_dwordx4 v[32:35], v[32:33], off
	s_nop 0
	global_load_dwordx4 v[36:39], v[36:37], off
	s_nop 0
	global_load_dwordx4 v[40:43], v[40:41], off
	s_nop 0
	global_load_dwordx4 v[44:47], v[44:45], off
	s_nop 0
	global_load_dwordx4 v[48:51], v[48:49], off
	s_nop 0
	global_load_dwordx4 v[52:55], v[52:53], off
	s_nop 0
	global_load_dwordx4 v[56:59], v[56:57], off
	s_nop 0
	global_load_dwordx4 v[60:63], v[60:61], off
	s_nop 0
	global_load_dwordx4 v[64:67], v[64:65], off
	s_nop 0
	global_load_dwordx4 v[68:71], v[68:69], off
	s_nop 0
	global_load_dwordx4 v[72:75], v[72:73], off
	s_nop 0
	global_load_dwordx4 v[76:79], v[76:77], off
	s_nop 0
	global_load_dwordx4 v[80:83], v[80:81], off
	s_nop 0
	global_load_dwordx4 v[84:87], v[84:85], off
	s_nop 0
	global_load_dwordx4 v[88:91], v[88:89], off
	s_nop 0
	global_load_dwordx4 v[92:95], v[92:93], off
	s_nop 0
	global_load_dwordx4 v[96:99], v[96:97], off
	s_nop 0
	global_load_dwordx4 v[100:103], v[100:101], off
	s_nop 0
	global_load_dwordx4 v[104:107], v[104:105], off
	s_nop 0
	global_load_dwordx4 v[108:111], v[108:109], off
	s_nop 0
	global_load_dwordx4 v[112:115], v[112:113], off
	s_nop 0
	global_load_dwordx4 v[116:119], v[116:117], off
	s_nop 0
	global_load_dwordx4 v[120:123], v[120:121], off
	s_nop 0
	global_load_dwordx4 v[124:127], v[124:125], off
	s_nop 0
	global_load_dwordx4 v[156:159], v[128:129], off
	v_add_co_u32_e32 v152, vcc, s46, v150
	v_mov_b32_e32 v142, v149
	s_nop 0
	v_addc_co_u32_e32 v153, vcc, 0, v151, vcc
	v_mov_b32_e32 v143, v149
	s_waitcnt vmcnt(31)
; template <int MODE>
; __device__ __forceinline__ void tr_matrix6(const float* W, int nb, int K, int N, unsigned char* WT, int drows, int rot, int gw, int NGW, int lane, float wscale) {
;     ...
;         for (int j = 0; j < 4; ++j) { float x[32];
; #pragma unroll
;             for (int i = 0; i < 32; ++i) x[i] = v[i][j] * wscale;
	v_mul_f32_e32 v2, 0x42b40000, v2
	v_mul_f32_e32 v3, 0x42b40000, v3
	v_mul_f32_e32 v4, 0x42b40000, v4
	v_mul_f32_e32 v5, 0x42b40000, v5
	v_med3_f32 v2, v2, s45, v155
	s_waitcnt vmcnt(30)
	v_mul_f32_e32 v6, 0x42b40000, v8
	s_waitcnt vmcnt(29)
	v_mul_f32_e32 v7, 0x42b40000, v12
	s_waitcnt vmcnt(28)
	v_mul_f32_e32 v8, 0x42b40000, v16
	s_waitcnt vmcnt(27)
	v_mul_f32_e32 v12, 0x42b40000, v20
	s_waitcnt vmcnt(26)
	v_mul_f32_e32 v16, 0x42b40000, v24
	s_waitcnt vmcnt(25)
	v_mul_f32_e32 v20, 0x42b40000, v28
	v_mul_f32_e32 v24, 0x42b40000, v9
	v_mul_f32_e32 v28, 0x42b40000, v10
	v_mul_f32_e32 v128, 0x42b40000, v11
	s_waitcnt vmcnt(24)
	v_mul_f32_e32 v9, 0x42b40000, v32
	v_mul_f32_e32 v32, 0x42b40000, v13
	v_mul_f32_e32 v129, 0x42b40000, v14
	v_mul_f32_e32 v132, 0x42b40000, v15
	s_waitcnt vmcnt(23)
	v_mul_f32_e32 v10, 0x42b40000, v36
	v_mul_f32_e32 v36, 0x42b40000, v17
	s_waitcnt vmcnt(22)
	v_mul_f32_e32 v11, 0x42b40000, v40
	s_waitcnt vmcnt(21)
	v_mul_f32_e32 v13, 0x42b40000, v44
	s_waitcnt vmcnt(20)
	v_mul_f32_e32 v14, 0x42b40000, v48
	s_waitcnt vmcnt(19)
	v_mul_f32_e32 v15, 0x42b40000, v52
	v_mul_f32_e32 v137, 0x42b40000, v35
	s_waitcnt vmcnt(18)
	v_mul_f32_e32 v17, 0x42b40000, v56
	v_mul_f32_e32 v35, 0x42b40000, v37
	v_mul_f32_e32 v44, 0x42b40000, v38
	v_mul_f32_e32 v140, 0x42b40000, v39
	s_waitcnt vmcnt(17)
	v_mul_f32_e32 v37, 0x42b40000, v60
	v_mul_f32_e32 v38, 0x42b40000, v41
	v_mul_f32_e32 v48, 0x42b40000, v42
	v_mul_f32_e32 v141, 0x42b40000, v43
	s_waitcnt vmcnt(16)
	v_mul_f32_e32 v39, 0x42b40000, v64
	v_mul_f32_e32 v160, 0x42b40000, v47
	s_waitcnt vmcnt(15)
	v_mul_f32_e32 v41, 0x42b40000, v68
	v_mul_f32_e32 v42, 0x42b40000, v49
	v_mul_f32_e32 v161, 0x42b40000, v51
	s_waitcnt vmcnt(14)
	v_mul_f32_e32 v43, 0x42b40000, v72
	v_mul_f32_e32 v47, 0x42b40000, v53
	v_mul_f32_e32 v49, 0x42b40000, v54
	s_waitcnt vmcnt(13)
	v_mul_f32_e32 v51, 0x42b40000, v76
	v_mul_f32_e32 v163, 0x42b40000, v58
	v_mul_f32_e32 v164, 0x42b40000, v59
	s_waitcnt vmcnt(12)
	v_mul_f32_e32 v52, 0x42b40000, v80
	v_mul_f32_e32 v165, 0x42b40000, v61
	v_mul_f32_e32 v166, 0x42b40000, v62
	s_waitcnt vmcnt(11)
	v_mul_f32_e32 v53, 0x42b40000, v84
	s_waitcnt vmcnt(10)
	v_mul_f32_e32 v54, 0x42b40000, v88
	s_waitcnt vmcnt(9)
	v_mul_f32_e32 v56, 0x42b40000, v92
	s_waitcnt vmcnt(8)
	v_mul_f32_e32 v58, 0x42b40000, v96
	v_mul_f32_e32 v59, 0x42b40000, v77
	v_mul_f32_e32 v174, 0x42b40000, v78
	v_mul_f32_e32 v175, 0x42b40000, v79
	s_waitcnt vmcnt(7)
	v_mul_f32_e32 v60, 0x42b40000, v100
	v_mul_f32_e32 v61, 0x42b40000, v81
	s_waitcnt vmcnt(6)
	v_mul_f32_e32 v62, 0x42b40000, v104
	s_waitcnt vmcnt(5)
	v_mul_f32_e32 v76, 0x42b40000, v108
	s_waitcnt vmcnt(4)
	v_mul_f32_e32 v77, 0x42b40000, v112
	s_waitcnt vmcnt(3)
	v_mul_f32_e32 v78, 0x42b40000, v116
	s_waitcnt vmcnt(2)
	v_mul_f32_e32 v79, 0x42b40000, v120
	s_waitcnt vmcnt(1)
	v_mul_f32_e32 v80, 0x42b40000, v124
	s_waitcnt vmcnt(0)
	v_mul_f32_e32 v81, 0x42b40000, v156
	v_mul_f32_e32 v133, 0x42b40000, v18
	v_mul_f32_e32 v136, 0x42b40000, v19
	v_mul_f32_e32 v19, 0x42b40000, v21
	v_mul_f32_e32 v21, 0x42b40000, v22
	v_mul_f32_e32 v22, 0x42b40000, v23
	v_mul_f32_e32 v23, 0x42b40000, v25
	v_mul_f32_e32 v25, 0x42b40000, v26
	v_mul_f32_e32 v26, 0x42b40000, v27
	v_mul_f32_e32 v27, 0x42b40000, v29
	v_mul_f32_e32 v29, 0x42b40000, v30
	v_mul_f32_e32 v30, 0x42b40000, v31
	v_mul_f32_e32 v31, 0x42b40000, v33
	v_mul_f32_e32 v33, 0x42b40000, v34
	v_mul_f32_e32 v40, 0x42b40000, v45
	v_mul_f32_e32 v45, 0x42b40000, v46
	v_mul_f32_e32 v46, 0x42b40000, v50
	v_mul_f32_e32 v162, 0x42b40000, v55
	v_mul_f32_e32 v64, 0x42b40000, v57
	v_mul_f32_e32 v167, 0x42b40000, v63
	v_mul_f32_e32 v65, 0x42b40000, v65
	v_mul_f32_e32 v168, 0x42b40000, v66
	v_mul_f32_e32 v169, 0x42b40000, v67
	v_mul_f32_e32 v55, 0x42b40000, v69
	v_mul_f32_e32 v170, 0x42b40000, v70
	v_mul_f32_e32 v171, 0x42b40000, v71
	v_mul_f32_e32 v57, 0x42b40000, v73
	v_mul_f32_e32 v172, 0x42b40000, v74
	v_mul_f32_e32 v173, 0x42b40000, v75
	v_mul_f32_e32 v176, 0x42b40000, v82
	v_mul_f32_e32 v177, 0x42b40000, v83
	v_mul_f32_e32 v63, 0x42b40000, v85
	v_mul_f32_e32 v104, 0x42b40000, v86
	v_mul_f32_e32 v178, 0x42b40000, v87
	v_mul_f32_e32 v87, 0x42b40000, v89
	v_mul_f32_e32 v108, 0x42b40000, v90
	v_mul_f32_e32 v179, 0x42b40000, v91
	v_mul_f32_e32 v88, 0x42b40000, v93
	v_mul_f32_e32 v112, 0x42b40000, v94
	v_mul_f32_e32 v180, 0x42b40000, v95
	v_mul_f32_e32 v89, 0x42b40000, v97
	v_mul_f32_e32 v116, 0x42b40000, v98
	v_mul_f32_e32 v181, 0x42b40000, v99
	v_mul_f32_e32 v90, 0x42b40000, v101
	v_mul_f32_e32 v120, 0x42b40000, v102
	v_mul_f32_e32 v182, 0x42b40000, v103
	v_mul_f32_e32 v91, 0x42b40000, v105
	v_mul_f32_e32 v124, 0x42b40000, v106
	v_mul_f32_e32 v183, 0x42b40000, v107
	v_mul_f32_e32 v92, 0x42b40000, v109
	v_mul_f32_e32 v109, 0x42b40000, v110
	v_mul_f32_e32 v156, 0x42b40000, v111
	v_mul_f32_e32 v93, 0x42b40000, v113
	v_mul_f32_e32 v94, 0x42b40000, v117
	v_mul_f32_e32 v110, 0x42b40000, v114
	v_mul_f32_e32 v184, 0x42b40000, v115
	v_mul_f32_e32 v95, 0x42b40000, v121
	v_mul_f32_e32 v96, 0x42b40000, v125
	v_mul_f32_e32 v111, 0x42b40000, v118
	v_mul_f32_e32 v185, 0x42b40000, v119
	v_mul_f32_e32 v97, 0x42b40000, v157
	v_mul_f32_e32 v113, 0x42b40000, v122
	v_mul_f32_e32 v114, 0x42b40000, v126
; template <int MODE>
; __device__ __forceinline__ void tr_matrix6(const float* W, int nb, int K, int N, unsigned char* WT, int drows, int rot, int gw, int NGW, int lane, float wscale) {
;     ...
;         for (int j = 0; j < 4; ++j) { float x[32];
; #pragma unroll
;             for (int i = 0; i < 32; ++i) x[i] = v[i][j] * wscale;
;             const v6u w = pk32_fp6(x);
;             *(u32x4*)(dst + (size_t)j * K) = (u32x4){w[0], w[1], w[2], w[3]}; *(u32x4*)(dst + (size_t)j * K + 16) = (u32x4){w[4], w[5], 0u, 0u}; }
	v_mul_f32_e32 v157, 0x42b40000, v123
	v_mul_f32_e32 v115, 0x42b40000, v158
	v_mul_f32_e32 v158, 0x42b40000, v127
	v_mul_f32_e32 v159, 0x42b40000, v159
	v_med3_f32 v50, v3, s45, v155
	v_med3_f32 v34, v4, s45, v155
	v_med3_f32 v18, v5, s45, v155
	v_med3_f32 v3, v6, s45, v155
	v_med3_f32 v66, v41, s45, v155
	v_med3_f32 v67, v43, s45, v155
	v_med3_f32 v4, v7, s45, v155
	v_med3_f32 v68, v51, s45, v155
	v_med3_f32 v5, v8, s45, v155
	v_med3_f32 v69, v52, s45, v155
	v_med3_f32 v6, v12, s45, v155
	v_med3_f32 v70, v53, s45, v155
	v_med3_f32 v7, v16, s45, v155
	v_med3_f32 v71, v54, s45, v155
	v_med3_f32 v8, v20, s45, v155
	v_med3_f32 v72, v56, s45, v155
	v_med3_f32 v9, v9, s45, v155
	v_med3_f32 v73, v58, s45, v155
	v_med3_f32 v10, v10, s45, v155
	v_med3_f32 v74, v60, s45, v155
	v_med3_f32 v11, v11, s45, v155
	v_med3_f32 v75, v62, s45, v155
	v_med3_f32 v12, v13, s45, v155
	v_med3_f32 v76, v76, s45, v155
	v_med3_f32 v13, v14, s45, v155
	v_med3_f32 v77, v77, s45, v155
	v_med3_f32 v14, v15, s45, v155
	v_med3_f32 v78, v78, s45, v155
	v_med3_f32 v15, v17, s45, v155
	v_med3_f32 v79, v79, s45, v155
	v_med3_f32 v16, v37, s45, v155
	v_med3_f32 v80, v80, s45, v155
	v_med3_f32 v17, v39, s45, v155
	v_med3_f32 v81, v81, s45, v155
	v_med3_f32 v51, v24, s45, v155
	v_med3_f32 v82, v55, s45, v155
	v_med3_f32 v83, v57, s45, v155
	v_med3_f32 v52, v32, s45, v155
	v_med3_f32 v84, v59, s45, v155
	v_med3_f32 v53, v36, s45, v155
	v_med3_f32 v85, v61, s45, v155
	v_med3_f32 v54, v19, s45, v155
	v_med3_f32 v86, v63, s45, v155
	v_med3_f32 v55, v23, s45, v155
	v_med3_f32 v87, v87, s45, v155
	v_med3_f32 v56, v27, s45, v155
	v_med3_f32 v88, v88, s45, v155
	v_med3_f32 v57, v31, s45, v155
	v_med3_f32 v89, v89, s45, v155
	v_med3_f32 v58, v35, s45, v155
	v_med3_f32 v90, v90, s45, v155
	v_med3_f32 v59, v38, s45, v155
	v_med3_f32 v91, v91, s45, v155
	v_med3_f32 v60, v40, s45, v155
	v_med3_f32 v92, v92, s45, v155
	v_med3_f32 v61, v42, s45, v155
	v_med3_f32 v93, v93, s45, v155
	v_med3_f32 v62, v47, s45, v155
	v_med3_f32 v94, v94, s45, v155
	v_med3_f32 v63, v64, s45, v155
	v_med3_f32 v95, v95, s45, v155
	v_med3_f32 v64, v165, s45, v155
	v_med3_f32 v96, v96, s45, v155
	v_med3_f32 v65, v65, s45, v155
	v_med3_f32 v97, v97, s45, v155
	v_med3_f32 v35, v28, s45, v155
	v_med3_f32 v98, v170, s45, v155
	v_med3_f32 v99, v172, s45, v155
	v_med3_f32 v36, v129, s45, v155
	v_med3_f32 v100, v174, s45, v155
	v_med3_f32 v37, v133, s45, v155
	v_med3_f32 v101, v176, s45, v155
	v_med3_f32 v38, v21, s45, v155
	v_med3_f32 v102, v104, s45, v155
	v_med3_f32 v39, v25, s45, v155
	v_med3_f32 v103, v108, s45, v155
	v_med3_f32 v40, v29, s45, v155
	v_med3_f32 v104, v112, s45, v155
	v_med3_f32 v41, v33, s45, v155
	v_med3_f32 v105, v116, s45, v155
	v_med3_f32 v42, v44, s45, v155
	v_med3_f32 v106, v120, s45, v155
	v_med3_f32 v43, v48, s45, v155
	v_med3_f32 v107, v124, s45, v155
	v_med3_f32 v44, v45, s45, v155
	v_med3_f32 v108, v109, s45, v155
	v_med3_f32 v45, v46, s45, v155
	v_med3_f32 v109, v110, s45, v155
	v_med3_f32 v46, v49, s45, v155
	v_med3_f32 v110, v111, s45, v155
	v_med3_f32 v47, v163, s45, v155
	v_med3_f32 v111, v113, s45, v155
	v_med3_f32 v48, v166, s45, v155
	v_med3_f32 v112, v114, s45, v155
	v_med3_f32 v49, v168, s45, v155
	v_med3_f32 v113, v115, s45, v155
	v_med3_f32 v19, v128, s45, v155
	v_med3_f32 v114, v171, s45, v155
	v_med3_f32 v115, v173, s45, v155
	v_med3_f32 v20, v132, s45, v155
	v_med3_f32 v116, v175, s45, v155
	v_med3_f32 v21, v136, s45, v155
	v_med3_f32 v117, v177, s45, v155
	v_med3_f32 v22, v22, s45, v155
	v_med3_f32 v118, v178, s45, v155
	v_med3_f32 v23, v26, s45, v155
	v_med3_f32 v119, v179, s45, v155
	v_med3_f32 v24, v30, s45, v155
	v_med3_f32 v120, v180, s45, v155
	v_med3_f32 v25, v137, s45, v155
	v_med3_f32 v121, v181, s45, v155
	v_med3_f32 v26, v140, s45, v155
	v_med3_f32 v122, v182, s45, v155
	v_med3_f32 v27, v141, s45, v155
	v_med3_f32 v123, v183, s45, v155
	v_med3_f32 v28, v160, s45, v155
	v_med3_f32 v124, v156, s45, v155
	v_med3_f32 v29, v161, s45, v155
	v_med3_f32 v125, v184, s45, v155
	v_med3_f32 v30, v162, s45, v155
	v_med3_f32 v126, v185, s45, v155
	v_med3_f32 v31, v164, s45, v155
	v_med3_f32 v127, v157, s45, v155
	v_med3_f32 v32, v167, s45, v155
	v_med3_f32 v128, v158, s45, v155
	v_med3_f32 v33, v169, s45, v155
	v_med3_f32 v129, v159, s45, v155
	v_cvt_scalef32_2xpk16_fp6_f32 v[2:7], v[2:17], v[66:81], 1.0
	v_cvt_scalef32_2xpk16_fp6_f32 v[8:13], v[50:65], v[82:97], 1.0
	v_cvt_scalef32_2xpk16_fp6_f32 v[34:39], v[34:49], v[98:113], 1.0
	v_cvt_scalef32_2xpk16_fp6_f32 v[14:19], v[18:33], v[114:129], 1.0
	v_mov_b32_e32 v128, v6
	v_mov_b32_e32 v129, v7
	global_store_dwordx4 v[150:151], v[2:5], off
	global_store_dwordx4 v[150:151], v[8:11], off offset:2048
	v_mov_b32_e32 v132, v12
	v_mov_b32_e32 v133, v13
	global_store_dwordx4 v[152:153], v[34:37], off
	v_mov_b32_e32 v136, v38
	v_mov_b32_e32 v137, v39
	global_store_dwordx4 v[152:153], v[14:17], off offset:2048
	v_mov_b32_e32 v140, v18
	v_mov_b32_e32 v141, v19
	global_store_dwordx4 v[150:151], v[128:131], off offset:16
	global_store_dwordx4 v[150:151], v[132:135], off offset:2064
	global_store_dwordx4 v[152:153], v[136:139], off offset:16
	global_store_dwordx4 v[152:153], v[140:143], off offset:2064
	s_cbranch_scc1 .LBB0_58

;     ...
;     const int tid = opaque_tid(), wid = __builtin_amdgcn_readfirstlane(tid >> 6), lane = tid & 63, wr = wid >> 2, wc = wid & 3, fr = lane & 15, fq = lane >> 4;
;     const int K = g.K, nt = K / 128;
;     unsigned voffA[2], voffB[2];
; #pragma unroll
;     for (int i = 0; i < 2; ++i) { int R, C; stage_rc8(tid * 16 + i * 8192, R, C); const int Rb = Epi::PERM ? ((R & ~31) + perm32(R & 31)) : R;
;         voffA[i] = (unsigned)(R * g.lda + C); voffB[i] = (unsigned)(Rb * g.ldb + C); }
;     const size_t kstep = 128;
;     const size_t hstepA = (size_t)HALF * g.lda, hstepB = (size_t)HALF * g.ldb;
;     const unsigned ldsw = (unsigned)wid * 1024u;
;     const int aoff0 = lds_byte8(wr * 64 + fr, 2 * fq), aoff1 = lds_byte8(wr * 64 + fr, 2 * fq + 1), boff0 = lds_byte8(wc * 32 + fr, 2 * fq), boff1 = lds_byte8(wc * 32 + fr, 2 * fq + 1);
;     ...
;     Unit cur, nxt; int ui = 0;
;     if (!S.next(0, cur)) return;
;     Acc acc;
; #pragma unroll
;     for (int a = 0; a < 2; ++a)
; #pragma unroll
;         for (int b = 0; b < 2; ++b)
; #pragma unroll
;             for (int m = 0; m < 4; ++m)
; #pragma unroll
;                 for (int n = 0; n < 2; ++n) acc[a][b][m][n] = (f32x4){0.f, 0.f, 0.f, 0.f};
;     typename Frag8<FP6>::T At[4], B0[2], B1[2];
;     const char* cA = (const char*)g.A + cur.aoff; const char* cB = (const char*)g.Bt + cur.boff;
;     S.a_ready(cur);
;     PG8_STAGE(PG8_SB(0, 0), cB, voffB); PG8_STAGE(PG8_SB(0, 1), cB + hstepB, voffB); PG8_STAGE(PG8_SA(0, 0), cA, voffA); PG8_STAGE(PG8_SA(0, 1), cA + hstepA, voffA);
;     if (wr == 1) PG8_BAR;
;     PG8_WAIT_V(2); PG8_BAR;
;     PG8_STAGE(PG8_SB(1, 0), cB + kstep, voffB); PG8_STAGE(PG8_SA(1, 0), cA + kstep, voffA); PG8_STAGE(PG8_SB(1, 1), cB + hstepB + kstep, voffB);
;     PG8_WAIT_V(6); PG8_BAR;
; template <int MODE>
; __device__ __forceinline__ void tr_matrix6(const float* W, int nb, int K, int N, unsigned char* WT, int drows, int rot, int gw, int NGW, int lane, float wscale) {
;     const int nbn = N / 32, per = (K / 256) * nbn, total = nb * per;
;     int it = gw - rot; if (it < 0) it += NGW;
;     const int c = lane & 7, q = lane >> 3;
;     for (; it < total; it += NGW) {
;         const int e = it / per, r = it - e * per, kb = r / nbn, nbk = r - kb * nbn, n0 = nbk * 32, k0 = kb * 256;
;         const float* src = W + (size_t)e * K * N + (size_t)(k0 + 32 * q) * N + n0 + 4 * c;
;         f32x4 v[32];
.LBB0_585:
	s_or_b64 exec, exec, s[4:5]
	v_mov_b32_e32 v12, v0
	s_waitcnt lgkmcnt(0)
	s_barrier
	v_readlane_b32 s98, v251, 9
	v_readlane_b32 s100, v251, 0
	v_readlane_b32 s101, v251, 1
	v_mbcnt_lo_u32_b32 v248, -1, 0
	v_mbcnt_hi_u32_b32 v248, -1, v248
	s_nop 3
	s_sub_u32 s100, s100, 0x38
	s_subb_u32 s101, s101, 0
	s_lshr_b32 s4, s98, 10
	s_lshl_b32 s5, s4, 3
	s_add_u32 s100, s100, s5
	s_addc_u32 s101, s101, 0
	s_load_dwordx2 s[100:101], s[100:101], 0x0
	s_lshr_b32 s6, s98, 3
	s_and_b32 s6, s6, 63
	s_lshr_b32 s8, s98, 9
	s_and_b32 s8, s8, 1
	s_add_u32 s8, s8, 2
	s_and_b32 s10, s98, 7
	s_mul_i32 s10, s10, 14
	s_lshl_b32 s5, s8, 11
	s_lshl_b32 s99, s6, 5
	s_add_u32 s5, s5, s99
	s_mul_i32 s5, s5, 0x7000
	s_lshl_b32 s99, s10, 8
	s_add_u32 s5, s5, s99
	s_waitcnt lgkmcnt(0)
	s_add_u32 s100, s100, s5
	s_addc_u32 s101, s101, 0
	v_writelane_b32 v252, s100, 4
	v_writelane_b32 v252, s101, 5
	s_lshl_b32 s4, s4, 7
	s_mul_i32 s5, s8, 0x3800
	s_add_u32 s4, s4, s5
	s_lshr_b32 s5, s10, 1
	s_lshl_b32 s5, s5, 8
	s_add_u32 s4, s4, s5
	s_lshl_b32 s4, s4, 11
	s_lshl_b32 s5, s6, 5
	s_add_u32 s4, s4, s5
	s_add_u32 s4, s4, 0x8a00000
	s_add_u32 s100, s70, s4
	s_addc_u32 s101, s71, 0
	v_writelane_b32 v252, s100, 6
	v_writelane_b32 v252, s101, 7
	v_lshlrev_b32_e32 v249, 11, v248
	v_lshlrev_b32_e32 v248, 2, v248
	v_mov_b32_e32 v254, 0x40f00000
	v_mov_b32_e32 v255, 0xc0f00000
	v_mov_b32_e32 v246, 0
	v_mov_b32_e32 v247, 0
	s_mov_b32 s98, 0
	s_cmpk_lt_i32 s2, 0xe00
	s_nop 0
	v_readfirstlane_b32 s1, v12
	s_cbranch_scc0 .LBB0_601
	v_lshlrev_b32_e32 v2, 4, v12
	v_add_u32_e32 v3, 0x2000, v2
	v_ashrrev_i32_e32 v10, 7, v3
	v_bfe_u32 v5, v3, 7, 2
	s_mov_b32 s4, 0x1fffe0
	v_and_or_b32 v5, v10, s4, v5
	v_bfe_u32 v11, v3, 7, 4
	s_mov_b32 s4, 0x1ffff0
	v_ashrrev_i32_e32 v13, 3, v12
	v_bfe_u32 v14, v2, 7, 4
	v_and_or_b32 v7, v10, s4, v11
	v_and_or_b32 v8, v13, s4, v14
	s_lshr_b32 s4, s3, 29
	s_add_i32 s4, s2, s4
	s_ashr_i32 s8, s1, 6
	s_ashr_i32 s6, s4, 3
	s_and_b32 s4, s4, -8
	s_ashr_i32 s5, s1, 8
	s_lshl_b32 s0, s8, 10
	s_sub_i32 s4, s2, s4
	s_cmp_lt_i32 s4, 0
	s_movk_i32 s10, 0x1c1
	s_cselect_b32 s7, s10, 0x1c0
	s_mul_i32 s4, s4, s7
	s_add_i32 s4, s4, s6
	s_mul_hi_i32 s6, s4, 0x92492493
	s_add_i32 s6, s6, s4
	s_lshr_b32 s7, s6, 31
	s_ashr_i32 s6, s6, 8
	s_add_i32 s6, s6, s7
	s_lshl_b32 s7, s6, 3
	s_mulk_i32 s6, 0x1c0
	s_sub_i32 s6, s4, s6
	s_sext_i32_i16 s4, s6
	v_lshrrev_b32_e32 v4, 7, v3
	v_lshrrev_b32_e32 v6, 2, v10
	v_lshrrev_b32_e32 v3, 6, v3
	s_bfe_u32 s4, s4, 0x3001c
	v_and_b32_e32 v6, 4, v6
	v_and_b32_e32 v3, 24, v3
	s_add_i32 s9, s6, s4
	v_or3_b32 v3, v5, v6, v3
	v_bfe_u32 v5, v4, 3, 1
	s_sext_i32_i16 s4, s9
	s_and_b32 s9, s9, 0xfff8
	v_and_or_b32 v4, v4, 6, v5
	s_sub_i32 s6, s6, s9
	v_lshlrev_b32_e32 v3, 11, v3
	v_lshlrev_b32_e32 v4, 4, v4
	v_and_b32_e32 v5, 0x70, v2
	s_sext_i32_i16 s6, s6
	v_bitop3_b32 v162, v3, v4, v5 bitop3:0xf6
	v_lshlrev_b32_e32 v3, 11, v7
	s_lshr_b32 s4, s4, 3
	s_add_i32 s56, s7, s6
	v_bitop3_b32 v164, v4, v3, v5 bitop3:0xde
	v_bfe_u32 v3, v12, 3, 25
	v_and_b32_e32 v6, 0x1fffe0, v13
	v_lshrrev_b32_e32 v7, 2, v13
	v_lshrrev_b32_e32 v9, 2, v12
	s_bfe_i64 s[6:7], s[4:5], 0x100000
	s_ashr_i32 s57, s56, 31
	v_and_or_b32 v6, v3, 3, v6
	v_and_b32_e32 v7, 4, v7
	v_and_b32_e32 v9, 24, v9
	s_lshl_b64 s[6:7], s[6:7], 19
	s_lshl_b64 s[12:13], s[56:57], 19
	v_readlane_b32 s9, v251, 51
	v_or3_b32 v6, v6, v7, v9
	v_bfe_u32 v7, v3, 3, 1
	s_add_u32 s58, s9, s6
	v_readlane_b32 s6, v251, 52
	v_and_or_b32 v3, v3, 6, v7
	s_addc_u32 s59, s6, s7
	s_add_i32 s11, s0, 0
	v_lshlrev_b32_e32 v6, 11, v6
	v_lshlrev_b32_e32 v3, 4, v3
	s_add_i32 s24, s11, 0x10000
	s_add_i32 s25, s11, 0x12000
	v_bitop3_b32 v166, v6, v3, v5 bitop3:0xf6
	s_mov_b32 m0, s24
	s_add_u32 s6, s58, 0x40000
	global_load_lds_dwordx4 v166, s[58:59]
	s_mov_b32 m0, s25
	s_addc_u32 s7, s59, 0
	s_add_i32 s66, s11, 0x14000
	s_add_i32 s67, s11, 0x16000
	global_load_lds_dwordx4 v162, s[58:59]
	s_mov_b32 m0, s66
	s_add_u32 s60, s14, s12
	v_lshlrev_b32_e32 v6, 11, v8
	global_load_lds_dwordx4 v166, s[6:7]
	s_mov_b32 m0, s67
	s_addc_u32 s61, s15, s13
	s_add_i32 s0, s11, 0x2000
	v_bitop3_b32 v168, v3, v6, v5 bitop3:0xde
	global_load_lds_dwordx4 v162, s[6:7]
	s_mov_b32 m0, s11
	s_add_u32 s6, s60, 0x40000
	global_load_lds_dwordx4 v168, s[60:61]
	s_mov_b32 m0, s0
	s_addc_u32 s7, s61, 0
	s_add_i32 s78, s11, 0x4000
	global_load_lds_dwordx4 v164, s[60:61]
	s_mov_b32 m0, s78
	s_add_i32 s79, s11, 0x6000
	global_load_lds_dwordx4 v168, s[6:7]
	s_mov_b32 m0, s79
	v_mov_b32_e32 v167, 0
	global_load_lds_dwordx4 v164, s[6:7]
	s_movk_i32 s6, 0x70
	v_mov_b32_e32 v163, v167
	v_mov_b32_e32 v169, v167
	v_mov_b32_e32 v165, v167
	s_cmp_eq_u32 s5, 1
	v_bitop3_b32 v15, v4, v2, s6 bitop3:0x78
	v_bitop3_b32 v16, v3, v2, s6 bitop3:0x78
	s_mov_b32 s80, 0
	v_lshl_add_u64 v[8:9], s[58:59], 0, v[166:167]
	v_lshl_add_u64 v[6:7], s[58:59], 0, v[162:163]
	v_lshl_add_u64 v[2:3], s[60:61], 0, v[168:169]
	s_cselect_b64 s[6:7], -1, 0
	s_cmp_lg_u32 s5, 1
	v_lshl_add_u64 v[4:5], s[60:61], 0, v[164:165]
	s_cbranch_scc1 .LBB0_588
	s_barrier

;     __device__ __forceinline__ void operator()(const Acc& acc, const Unit& u, int wr, int wc, int fr, int fq) const {
;         const int row0 = u.pm * BM + wr * 64 + fr, col0 = u.pn * HALF + wc * 32 + 8 * fq;
;         const float k_ = in_scale * in_scale * out_scale, c1 = -in_scale * 1.4426950408889634f, c0 = -__builtin_log2f(k_), c3 = 1.0f / k_;
; #pragma unroll
;         for (int ai = 0; ai < 2; ++ai)
; #pragma unroll
;             for (int m = 0; m < 4; ++m) { const size_t off = (size_t)(row0 + ai * HALF + m * 16) * ldc + col0;
;                 float h[8];
; #pragma unroll
;                 for (int n = 0; n < 2; ++n)
; #pragma unroll
;                     for (int e = 0; e < 4; ++e) { const float a0 = acc[ai][0][m][n][e], a1 = acc[ai][1][m][n][e];
;                         h[n * 4 + e] = (a0 * a1) * __builtin_amdgcn_rcpf(c3 + __builtin_amdgcn_exp2f(fmaf(a0, c1, c0))); }
;     ...
;         if constexpr (MODE == 2) {
; #pragma unroll
;             for (int a = 0; a < 2; ++a)
; #pragma unroll
;                 for (int b = 0; b < 2; ++b)
; #pragma unroll
;                     for (int m = 0; m < 4; ++m)
; #pragma unroll
;                         for (int n = 0; n < 2; ++n)
;                         { const f32x4 t_ = acc[a][b][m][n]; f32x4 r_;
;                           r_.x = (float)__float_as_int(t_.x); r_.y = (float)__float_as_int(t_.y); r_.z = (float)__float_as_int(t_.z); r_.w = (float)__float_as_int(t_.w); acc[a][b][m][n] = r_; }
;         }
.LBB0_597:
	s_cmp_lt_u32 s98, 14
	s_cbranch_scc0 .Lp8f_s
	v_readlane_b32 s100, v252, 4
	v_readlane_b32 s101, v252, 5
	s_lshl_b32 s99, s98, 8
	s_nop 1
	s_add_u32 s100, s100, s99
	s_addc_u32 s101, s101, 0
	global_load_dword v208, v248, s[100:101]
	s_add_u32 s100, s100, 0x7000
	s_addc_u32 s101, s101, 0
	global_load_dword v209, v248, s[100:101]
	s_add_u32 s100, s100, 0x7000
	s_addc_u32 s101, s101, 0
	global_load_dword v210, v248, s[100:101]
	s_add_u32 s100, s100, 0x7000
	s_addc_u32 s101, s101, 0
	global_load_dword v211, v248, s[100:101]
	s_add_u32 s100, s100, 0x7000
	s_addc_u32 s101, s101, 0
	global_load_dword v212, v248, s[100:101]
	s_add_u32 s100, s100, 0x7000
	s_addc_u32 s101, s101, 0
	global_load_dword v213, v248, s[100:101]
	s_add_u32 s100, s100, 0x7000
	s_addc_u32 s101, s101, 0
	global_load_dword v214, v248, s[100:101]
	s_add_u32 s100, s100, 0x7000
	s_addc_u32 s101, s101, 0
	global_load_dword v215, v248, s[100:101]
	s_add_u32 s100, s100, 0x7000
	s_addc_u32 s101, s101, 0
	global_load_dword v216, v248, s[100:101]
	s_add_u32 s100, s100, 0x7000
	s_addc_u32 s101, s101, 0
	global_load_dword v217, v248, s[100:101]
	s_add_u32 s100, s100, 0x7000
	s_addc_u32 s101, s101, 0
	global_load_dword v218, v248, s[100:101]
	s_add_u32 s100, s100, 0x7000
	s_addc_u32 s101, s101, 0
	global_load_dword v219, v248, s[100:101]
	s_add_u32 s100, s100, 0x7000
	s_addc_u32 s101, s101, 0
	global_load_dword v220, v248, s[100:101]
	s_add_u32 s100, s100, 0x7000
	s_addc_u32 s101, s101, 0
	global_load_dword v221, v248, s[100:101]
	s_add_u32 s100, s100, 0x7000
	s_addc_u32 s101, s101, 0
	global_load_dword v222, v248, s[100:101]
	s_add_u32 s100, s100, 0x7000
	s_addc_u32 s101, s101, 0
	global_load_dword v223, v248, s[100:101]
	s_add_u32 s100, s100, 0x7000
	s_addc_u32 s101, s101, 0
	global_load_dword v224, v248, s[100:101]
	s_add_u32 s100, s100, 0x7000
	s_addc_u32 s101, s101, 0
	global_load_dword v225, v248, s[100:101]
	s_add_u32 s100, s100, 0x7000
	s_addc_u32 s101, s101, 0
	global_load_dword v226, v248, s[100:101]
	s_add_u32 s100, s100, 0x7000
	s_addc_u32 s101, s101, 0
	global_load_dword v227, v248, s[100:101]
	s_add_u32 s100, s100, 0x7000
	s_addc_u32 s101, s101, 0
	global_load_dword v228, v248, s[100:101]
	s_add_u32 s100, s100, 0x7000
	s_addc_u32 s101, s101, 0
	global_load_dword v229, v248, s[100:101]
	s_add_u32 s100, s100, 0x7000
	s_addc_u32 s101, s101, 0
	global_load_dword v230, v248, s[100:101]
	s_add_u32 s100, s100, 0x7000
	s_addc_u32 s101, s101, 0
	global_load_dword v231, v248, s[100:101]
	s_add_u32 s100, s100, 0x7000
	s_addc_u32 s101, s101, 0
	global_load_dword v232, v248, s[100:101]
	s_add_u32 s100, s100, 0x7000
	s_addc_u32 s101, s101, 0
	global_load_dword v233, v248, s[100:101]
	s_add_u32 s100, s100, 0x7000
	s_addc_u32 s101, s101, 0
	global_load_dword v234, v248, s[100:101]
	s_add_u32 s100, s100, 0x7000
	s_addc_u32 s101, s101, 0
	global_load_dword v235, v248, s[100:101]
	s_add_u32 s100, s100, 0x7000
	s_addc_u32 s101, s101, 0
	global_load_dword v236, v248, s[100:101]
	s_add_u32 s100, s100, 0x7000
	s_addc_u32 s101, s101, 0
	global_load_dword v237, v248, s[100:101]
	s_add_u32 s100, s100, 0x7000
	s_addc_u32 s101, s101, 0
	global_load_dword v238, v248, s[100:101]
	s_add_u32 s100, s100, 0x7000
	s_addc_u32 s101, s101, 0
	global_load_dword v239, v248, s[100:101]
.Lp8f_s:
	v_cvt_f32_i32_e32 v126, v126
	v_cvt_f32_i32_e32 v127, v127
	v_cvt_f32_i32_e32 v128, v128
	v_cvt_f32_i32_e32 v129, v129
	v_cvt_f32_i32_e32 v122, v122
	v_cvt_f32_i32_e32 v141, v92
	v_cvt_f32_i32_e32 v92, v87
	v_cvt_f32_i32_e32 v87, v66
	v_cvt_f32_i32_e32 v66, v60
	v_cvt_f32_i32_e32 v60, v55
	v_cvt_f32_i32_e32 v55, v26
	v_cvt_f32_i32_e32 v26, v22
	v_cvt_f32_i32_e32 v22, v23
	v_cvt_f32_i32_e32 v23, v7
	v_cvt_f32_i32_e32 v7, v5
	v_fmamk_f32 v5, v126, 0xb80b6d22, v206
	v_cvt_f32_i32_e32 v123, v123
	v_cvt_f32_i32_e32 v136, v100
	v_cvt_f32_i32_e32 v100, v95
	v_cvt_f32_i32_e32 v95, v70
	v_cvt_f32_i32_e32 v70, v58
	v_cvt_f32_i32_e32 v58, v56
	v_cvt_f32_i32_e32 v56, v57
	v_cvt_f32_i32_e32 v57, v37
	v_cvt_f32_i32_e32 v37, v10
	v_cvt_f32_i32_e32 v10, v15
	v_exp_f32_e32 v5, v5
	v_fmamk_f32 v15, v127, 0xb80b6d22, v206
	v_cvt_f32_i32_e32 v124, v124
	v_cvt_f32_i32_e32 v143, v82
	v_cvt_f32_i32_e32 v82, v80
	v_cvt_f32_i32_e32 v80, v81
	v_cvt_f32_i32_e32 v81, v69
	v_cvt_f32_i32_e32 v69, v43
	v_cvt_f32_i32_e32 v43, v39
	v_cvt_f32_i32_e32 v39, v21
	v_cvt_f32_i32_e32 v21, v8
	v_cvt_f32_i32_e32 v8, v16
	v_exp_f32_e32 v15, v15
	v_fmamk_f32 v16, v128, 0xb80b6d22, v206
	v_cvt_f32_i32_e32 v125, v125
	v_cvt_f32_i32_e32 v139, v90
	v_cvt_f32_i32_e32 v90, v88
	v_cvt_f32_i32_e32 v88, v89
	v_cvt_f32_i32_e32 v89, v73
	v_cvt_f32_i32_e32 v73, v53
	v_cvt_f32_i32_e32 v53, v27
	v_cvt_f32_i32_e32 v27, v6
	v_cvt_f32_i32_e32 v6, v17
	v_exp_f32_e32 v16, v16
	v_fmamk_f32 v17, v129, 0xb80b6d22, v206
	v_cvt_f32_i32_e32 v142, v93
	v_cvt_f32_i32_e32 v93, v71
	v_cvt_f32_i32_e32 v71, v42
	v_cvt_f32_i32_e32 v42, v20
	v_cvt_f32_i32_e32 v20, v24
	v_exp_f32_e32 v17, v17
	v_fmamk_f32 v24, v122, 0xb80b6d22, v206
	v_cvt_f32_i32_e32 v114, v114
	v_cvt_f32_i32_e32 v138, v110
	v_cvt_f32_i32_e32 v110, v102
	v_cvt_f32_i32_e32 v102, v94
	v_cvt_f32_i32_e32 v94, v86
	v_cvt_f32_i32_e32 v86, v78
	v_cvt_f32_i32_e32 v78, v62
	v_cvt_f32_i32_e32 v62, v54
	v_cvt_f32_i32_e32 v54, v46
	v_cvt_f32_i32_e32 v46, v18
	v_cvt_f32_i32_e32 v18, v25
	v_add_f32_e32 v5, 0x4ce089af, v5
	v_exp_f32_e32 v24, v24
	v_fmamk_f32 v25, v123, 0xb80b6d22, v206
	v_cvt_f32_i32_e32 v115, v115
	v_cvt_f32_i32_e32 v133, v109
	v_cvt_f32_i32_e32 v109, v83
	v_cvt_f32_i32_e32 v83, v68
	v_cvt_f32_i32_e32 v68, v59
	v_cvt_f32_i32_e32 v59, v36
	v_cvt_f32_i32_e32 v36, v30
	v_cvt_f32_i32_e32 v30, v32
	v_rcp_f32_e32 v5, v5
; __device__ __forceinline__ unsigned pk4_i8(float a, float b, float c, float d) {
;     const unsigned ua = __float_as_uint(__builtin_amdgcn_fmed3f(a, -127.f, 127.f) + 12582912.f), ub = __float_as_uint(__builtin_amdgcn_fmed3f(b, -127.f, 127.f) + 12582912.f);
;     const unsigned uc = __float_as_uint(__builtin_amdgcn_fmed3f(c, -127.f, 127.f) + 12582912.f), ud = __float_as_uint(__builtin_amdgcn_fmed3f(d, -127.f, 127.f) + 12582912.f);
;     const unsigned t1 = __builtin_amdgcn_perm(ub, ua, 0x0c0c0400u), t2 = __builtin_amdgcn_perm(ud, uc, 0x0c0c0400u);
;     return __builtin_amdgcn_perm(t2, t1, 0x05040100u); }
;     __device__ __forceinline__ void operator()(const Acc& acc, const Unit& u, int wr, int wc, int fr, int fq) const {
;     ...
;         const float k_ = in_scale * in_scale * out_scale, c1 = -in_scale * 1.4426950408889634f, c0 = -__builtin_log2f(k_), c3 = 1.0f / k_;
; #pragma unroll
;         for (int ai = 0; ai < 2; ++ai)
; #pragma unroll
;             for (int m = 0; m < 4; ++m) { const size_t off = (size_t)(row0 + ai * HALF + m * 16) * ldc + col0;
;                 float h[8];
; #pragma unroll
;                 for (int n = 0; n < 2; ++n)
; #pragma unroll
;                     for (int e = 0; e < 4; ++e) { const float a0 = acc[ai][0][m][n][e], a1 = acc[ai][1][m][n][e];
;                         h[n * 4 + e] = (a0 * a1) * __builtin_amdgcn_rcpf(c3 + __builtin_amdgcn_exp2f(fmaf(a0, c1, c0))); }
;                 if constexpr (FP8OUT == 2) { u32x2 w; w.x = pk4_i8(h[0], h[1], h[2], h[3]); w.y = pk4_i8(h[4], h[5], h[6], h[7]); *(u32x2*)((unsigned char*)H + off) = w; }
	v_add_f32_e32 v15, 0x4ce089af, v15
	v_exp_f32_e32 v25, v25
	v_fmamk_f32 v32, v124, 0xb80b6d22, v206
	v_cvt_f32_i32_e32 v116, v116
	v_cvt_f32_i32_e32 v134, v98
	v_cvt_f32_i32_e32 v98, v96
	v_cvt_f32_i32_e32 v96, v97
	v_cvt_f32_i32_e32 v97, v77
	v_cvt_f32_i32_e32 v77, v51
	v_cvt_f32_i32_e32 v51, v28
	v_cvt_f32_i32_e32 v28, v33
	v_rcp_f32_e32 v15, v15
	v_add_f32_e32 v16, 0x4ce089af, v16
	v_exp_f32_e32 v32, v32
	v_fmamk_f32 v33, v125, 0xb80b6d22, v206
	v_cvt_f32_i32_e32 v117, v117
	v_rcp_f32_e32 v16, v16
	v_add_f32_e32 v17, 0x4ce089af, v17
	v_exp_f32_e32 v33, v33
	v_cvt_f32_i32_e32 v130, v106
	v_cvt_f32_i32_e32 v106, v104
	v_cvt_f32_i32_e32 v104, v105
	v_cvt_f32_i32_e32 v105, v85
	v_cvt_f32_i32_e32 v85, v67
	v_cvt_f32_i32_e32 v67, v44
	v_cvt_f32_i32_e32 v44, v19
	v_cvt_f32_i32_e32 v19, v9
	v_cvt_f32_i32_e32 v9, v4
	v_mul_f32_e32 v4, v114, v126
	v_rcp_f32_e32 v17, v17
	v_add_f32_e32 v24, 0x4ce089af, v24
	v_cvt_f32_i32_e32 v131, v107
	v_mul_f32_e32 v4, v5, v4
	v_mul_f32_e32 v5, v115, v127
	v_rcp_f32_e32 v24, v24
	v_add_f32_e32 v25, 0x4ce089af, v25
	v_cvt_f32_i32_e32 v132, v108
	v_mul_f32_e32 v5, v15, v5
	v_mul_f32_e32 v15, v116, v128
	v_rcp_f32_e32 v25, v25
	v_add_f32_e32 v32, 0x4ce089af, v32
	v_mul_f32_e32 v15, v16, v15
	v_mul_f32_e32 v16, v117, v129
	v_rcp_f32_e32 v32, v32
	v_add_f32_e32 v33, 0x4ce089af, v33
	v_mul_f32_e32 v16, v17, v16
	v_mul_f32_e32 v17, v130, v122
	v_rcp_f32_e32 v33, v33
	v_mul_f32_e32 v17, v24, v17
	v_mul_f32_e32 v24, v131, v123
	v_mul_f32_e32 v24, v25, v24
	v_mul_f32_e32 v25, v132, v124
	v_med3_f32 v4, v4, s1, v207
	v_med3_f32 v5, v5, s1, v207
	v_med3_f32 v15, v15, s1, v207
	v_med3_f32 v16, v16, s1, v207
	v_mul_f32_e32 v25, v32, v25
	v_mul_f32_e32 v32, v133, v125
	v_add_f32_e32 v4, 0x4b400000, v4
	v_add_f32_e32 v5, 0x4b400000, v5
	v_add_f32_e32 v15, 0x4b400000, v15
	v_add_f32_e32 v16, 0x4b400000, v16
	v_mul_f32_e32 v32, v33, v32
	v_perm_b32 v4, v5, v4, s33
	v_perm_b32 v5, v16, v15, s33
	v_perm_b32 v16, v5, v4, s87
	v_med3_f32 v4, v17, s1, v207
	v_med3_f32 v5, v24, s1, v207
	v_med3_f32 v15, v25, s1, v207
	v_med3_f32 v17, v32, s1, v207
	v_add_f32_e32 v4, 0x4b400000, v4
	v_add_f32_e32 v5, 0x4b400000, v5
	v_add_f32_e32 v15, 0x4b400000, v15
	v_add_f32_e32 v17, 0x4b400000, v17
	v_cvt_f32_i32_e32 v118, v118
	v_perm_b32 v4, v5, v4, s33
	v_perm_b32 v5, v17, v15, s33
	v_cvt_f32_i32_e32 v119, v119
	v_cvt_f32_i32_e32 v135, v99
	v_cvt_f32_i32_e32 v107, v84
	v_cvt_f32_i32_e32 v99, v76
	v_cvt_f32_i32_e32 v84, v79
	v_cvt_f32_i32_e32 v79, v50
	v_cvt_f32_i32_e32 v76, v63
	v_cvt_f32_i32_e32 v63, v34
	v_cvt_f32_i32_e32 v50, v48
	v_cvt_f32_i32_e32 v48, v29
	v_cvt_f32_i32_e32 v34, v31
	v_cvt_f32_i32_e32 v31, v12
	v_cvt_f32_i32_e32 v29, v13
	v_cvt_f32_i32_e32 v12, v14
	v_cvt_f32_i32_e32 v13, v2
	v_lshl_add_u32 v14, s56, 8, v186
	v_lshl_or_b32 v2, s57, 7, v203
	v_perm_b32 v17, v5, v4, s87
	v_mov_b64_e32 v[4:5], s[36:37]
	v_cvt_f32_i32_e32 v120, v120
	v_cvt_f32_i32_e32 v108, v103
	v_cvt_f32_i32_e32 v103, v74
	v_cvt_f32_i32_e32 v74, v64
	v_cvt_f32_i32_e32 v64, v61
	v_cvt_f32_i32_e32 v61, v35
	v_cvt_f32_i32_e32 v35, v11
	v_cvt_f32_i32_e32 v11, v3
	v_ashrrev_i32_e32 v3, 31, v2
	v_mad_i64_i32 v[24:25], s[8:9], v14, s88, v[4:5]
	v_cvt_f32_i32_e32 v121, v121
	v_lshl_add_u64 v[24:25], v[24:25], 0, v[2:3]
	global_store_dwordx2 v[24:25], v[16:17], off
	v_fmamk_f32 v17, v118, 0xb80b6d22, v206
	v_exp_f32_e32 v17, v17
	v_fmamk_f32 v24, v119, 0xb80b6d22, v206
	v_exp_f32_e32 v24, v24
	v_fmamk_f32 v25, v120, 0xb80b6d22, v206
	v_exp_f32_e32 v25, v25
	v_fmamk_f32 v32, v121, 0xb80b6d22, v206
	v_exp_f32_e32 v32, v32
	v_fmamk_f32 v33, v138, 0xb80b6d22, v206
	v_add_f32_e32 v17, 0x4ce089af, v17
	v_exp_f32_e32 v33, v33
	v_rcp_f32_e32 v17, v17
	v_add_f32_e32 v24, 0x4ce089af, v24
	v_rcp_f32_e32 v24, v24
	v_add_f32_e32 v25, 0x4ce089af, v25
	v_cvt_f32_i32_e32 v137, v101
	v_cvt_f32_i32_e32 v111, v111
	v_rcp_f32_e32 v25, v25
	v_add_f32_e32 v32, 0x4ce089af, v32
	v_cvt_f32_i32_e32 v112, v112
	v_mul_f32_e32 v16, v134, v118
	v_rcp_f32_e32 v32, v32
	v_add_f32_e32 v33, 0x4ce089af, v33
	v_cvt_f32_i32_e32 v140, v91
	v_cvt_f32_i32_e32 v113, v113
	v_mul_f32_e32 v16, v17, v16
	v_mul_f32_e32 v17, v135, v119
	v_rcp_f32_e32 v33, v33
	v_mul_f32_e32 v17, v24, v17
	v_mul_f32_e32 v24, v136, v120
	v_cvt_f32_i32_e32 v91, v72
	v_cvt_f32_i32_e32 v72, v65
	v_cvt_f32_i32_e32 v65, v45
	v_cvt_f32_i32_e32 v45, v38
	v_cvt_f32_i32_e32 v38, v41
	v_mul_f32_e32 v24, v25, v24
	v_mul_f32_e32 v25, v137, v121
	v_fmamk_f32 v41, v111, 0xb80b6d22, v206
	v_cvt_f32_i32_e32 v101, v75
	v_cvt_f32_i32_e32 v75, v52
	v_cvt_f32_i32_e32 v52, v47
	v_cvt_f32_i32_e32 v47, v49
	v_mul_f32_e32 v25, v32, v25
	v_mul_f32_e32 v32, v139, v138
	v_exp_f32_e32 v41, v41
	v_fmamk_f32 v49, v112, 0xb80b6d22, v206
	v_mul_f32_e32 v32, v33, v32
	v_mul_f32_e32 v33, v140, v111
	v_exp_f32_e32 v49, v49
	v_fmamk_f32 v111, v113, 0xb80b6d22, v206
	v_exp_f32_e32 v111, v111
	v_add_f32_e32 v41, 0x4ce089af, v41
	v_rcp_f32_e32 v41, v41
	v_add_f32_e32 v49, 0x4ce089af, v49
	v_rcp_f32_e32 v49, v49
	v_add_f32_e32 v111, 0x4ce089af, v111
	v_rcp_f32_e32 v111, v111
	v_mul_f32_e32 v33, v41, v33
	v_mul_f32_e32 v41, v141, v112
	v_med3_f32 v16, v16, s1, v207
	v_med3_f32 v17, v17, s1, v207
	v_med3_f32 v24, v24, s1, v207
	v_med3_f32 v25, v25, s1, v207
	v_mul_f32_e32 v41, v49, v41
	v_mul_f32_e32 v49, v142, v113
	v_add_f32_e32 v16, 0x4b400000, v16
	v_add_f32_e32 v17, 0x4b400000, v17
	v_add_f32_e32 v24, 0x4b400000, v24
	v_add_f32_e32 v25, 0x4b400000, v25
	v_mul_f32_e32 v49, v111, v49
	v_perm_b32 v16, v17, v16, s33
	v_perm_b32 v17, v25, v24, s33
	v_perm_b32 v16, v17, v16, s87
	v_med3_f32 v17, v32, s1, v207
	v_med3_f32 v24, v33, s1, v207
	v_med3_f32 v25, v41, s1, v207
; __device__ __forceinline__ unsigned cvtpk(float lo, float hi) { unsigned r; asm volatile("v_cvt_pk_bf16_f32 %0, %1, %2" : "=v"(r) : "v"(lo), "v"(hi)); return r; }
;     __device__ __forceinline__ void operator()(const Acc& acc, const Unit& u, int wr, int wc, int fr, int fq) const {
;     ...
;         for (int ai = 0; ai < 2; ++ai)
; #pragma unroll
;             for (int m = 0; m < 4; ++m) { const size_t off = (size_t)(row0 + ai * HALF + m * 16) * ldc + col0;
;                 float h[8];
; #pragma unroll
;                 for (int n = 0; n < 2; ++n)
; #pragma unroll
;                     for (int e = 0; e < 4; ++e) { const float a0 = acc[ai][0][m][n][e], a1 = acc[ai][1][m][n][e];
;                         h[n * 4 + e] = (a0 * a1) * __builtin_amdgcn_rcpf(c3 + __builtin_amdgcn_exp2f(fmaf(a0, c1, c0))); }
;                 if constexpr (FP8OUT == 2) { u32x2 w; w.x = pk4_i8(h[0], h[1], h[2], h[3]); w.y = pk4_i8(h[4], h[5], h[6], h[7]); *(u32x2*)((unsigned char*)H + off) = w; }
;                 else if constexpr (FP8OUT == 1) { u32x2 w; w.x = pk4_fp8_nc(h[0], h[1], h[2], h[3]); w.y = pk4_fp8_nc(h[4], h[5], h[6], h[7]); *(u32x2*)((unsigned char*)H + off) = w; }
;                 else { u32x4 w; w.x = cvtpk(h[0], h[1]); w.y = cvtpk(h[2], h[3]); w.z = cvtpk(h[4], h[5]); w.w = cvtpk(h[6], h[7]); *(u32x4*)((bf16_t*)H + off) = w; } }
	v_med3_f32 v32, v49, s1, v207
	v_add_f32_e32 v17, 0x4b400000, v17
	v_add_f32_e32 v24, 0x4b400000, v24
	v_add_f32_e32 v25, 0x4b400000, v25
	v_add_f32_e32 v32, 0x4b400000, v32
	v_or_b32_e32 v15, 16, v14
	v_perm_b32 v17, v24, v17, s33
	v_perm_b32 v24, v32, v25, s33
	v_perm_b32 v17, v24, v17, s87
	v_mad_i64_i32 v[24:25], s[8:9], v15, s88, v[4:5]
	v_lshl_add_u64 v[24:25], v[24:25], 0, v[2:3]
	global_store_dwordx2 v[24:25], v[16:17], off
	v_fmamk_f32 v17, v110, 0xb80b6d22, v206
	v_exp_f32_e32 v17, v17
	v_fmamk_f32 v24, v108, 0xb80b6d22, v206
	v_exp_f32_e32 v24, v24
	v_fmamk_f32 v25, v106, 0xb80b6d22, v206
	v_exp_f32_e32 v25, v25
	v_fmamk_f32 v32, v104, 0xb80b6d22, v206
	v_exp_f32_e32 v32, v32
	v_fmamk_f32 v33, v102, 0xb80b6d22, v206
	v_add_f32_e32 v17, 0x4ce089af, v17
	v_exp_f32_e32 v33, v33
	v_fmamk_f32 v41, v100, 0xb80b6d22, v206
	v_rcp_f32_e32 v17, v17
	v_add_f32_e32 v24, 0x4ce089af, v24
	v_exp_f32_e32 v41, v41
	v_fmamk_f32 v49, v98, 0xb80b6d22, v206
	v_rcp_f32_e32 v24, v24
	v_add_f32_e32 v25, 0x4ce089af, v25
	v_exp_f32_e32 v49, v49
	v_rcp_f32_e32 v25, v25
	v_add_f32_e32 v32, 0x4ce089af, v32
	v_mul_f32_e32 v16, v143, v110
	v_rcp_f32_e32 v32, v32
	v_add_f32_e32 v33, 0x4ce089af, v33
	v_mul_f32_e32 v16, v17, v16
	v_mul_f32_e32 v17, v109, v108
	v_rcp_f32_e32 v33, v33
	v_add_f32_e32 v41, 0x4ce089af, v41
	v_mul_f32_e32 v17, v24, v17
	v_mul_f32_e32 v24, v107, v106
	v_rcp_f32_e32 v41, v41
	v_add_f32_e32 v49, 0x4ce089af, v49
	v_mul_f32_e32 v24, v25, v24
	v_mul_f32_e32 v25, v105, v104
	v_rcp_f32_e32 v49, v49
	v_mul_f32_e32 v25, v32, v25
	v_mul_f32_e32 v32, v103, v102
	v_mul_f32_e32 v32, v33, v32
	v_mul_f32_e32 v33, v101, v100
	v_mul_f32_e32 v33, v41, v33
	v_mul_f32_e32 v41, v99, v98
	v_mul_f32_e32 v41, v49, v41
	v_mul_f32_e32 v49, v97, v96
	v_fmamk_f32 v96, v96, 0xb80b6d22, v206
	v_exp_f32_e32 v96, v96
	v_med3_f32 v16, v16, s1, v207
	v_med3_f32 v17, v17, s1, v207
	v_med3_f32 v24, v24, s1, v207
	v_add_f32_e32 v96, 0x4ce089af, v96
	v_rcp_f32_e32 v96, v96
	v_med3_f32 v25, v25, s1, v207
	v_add_f32_e32 v16, 0x4b400000, v16
	v_add_f32_e32 v17, 0x4b400000, v17
	v_add_f32_e32 v24, 0x4b400000, v24
	v_add_f32_e32 v25, 0x4b400000, v25
	v_mul_f32_e32 v49, v96, v49
	v_perm_b32 v16, v17, v16, s33
	v_perm_b32 v17, v25, v24, s33
	v_perm_b32 v16, v17, v16, s87
	v_med3_f32 v17, v32, s1, v207
	v_med3_f32 v24, v33, s1, v207
	v_med3_f32 v25, v41, s1, v207
	v_med3_f32 v32, v49, s1, v207
	v_add_f32_e32 v17, 0x4b400000, v17
	v_add_f32_e32 v24, 0x4b400000, v24
	v_add_f32_e32 v25, 0x4b400000, v25
	v_add_f32_e32 v32, 0x4b400000, v32
	v_or_b32_e32 v15, 32, v14
	v_perm_b32 v17, v24, v17, s33
	v_perm_b32 v24, v32, v25, s33
	v_perm_b32 v17, v24, v17, s87
	v_mad_i64_i32 v[24:25], s[8:9], v15, s88, v[4:5]
	v_lshl_add_u64 v[24:25], v[24:25], 0, v[2:3]
	global_store_dwordx2 v[24:25], v[16:17], off
	v_fmamk_f32 v17, v94, 0xb80b6d22, v206
	v_exp_f32_e32 v17, v17
	v_fmamk_f32 v24, v92, 0xb80b6d22, v206
	v_exp_f32_e32 v24, v24
	v_fmamk_f32 v25, v90, 0xb80b6d22, v206
	v_exp_f32_e32 v25, v25
	v_fmamk_f32 v32, v88, 0xb80b6d22, v206
	v_exp_f32_e32 v32, v32
	v_fmamk_f32 v33, v86, 0xb80b6d22, v206
	v_add_f32_e32 v17, 0x4ce089af, v17
	v_exp_f32_e32 v33, v33
	v_fmamk_f32 v41, v84, 0xb80b6d22, v206
	v_rcp_f32_e32 v17, v17
	v_add_f32_e32 v24, 0x4ce089af, v24
	v_exp_f32_e32 v41, v41
	v_fmamk_f32 v49, v82, 0xb80b6d22, v206
	v_rcp_f32_e32 v24, v24
	v_add_f32_e32 v25, 0x4ce089af, v25
	v_exp_f32_e32 v49, v49
	v_rcp_f32_e32 v25, v25
	v_add_f32_e32 v32, 0x4ce089af, v32
	v_mul_f32_e32 v16, v95, v94
	v_rcp_f32_e32 v32, v32
	v_add_f32_e32 v33, 0x4ce089af, v33
	v_mul_f32_e32 v16, v17, v16
	v_mul_f32_e32 v17, v93, v92
	v_rcp_f32_e32 v33, v33
	v_add_f32_e32 v41, 0x4ce089af, v41
	v_mul_f32_e32 v17, v24, v17
	v_mul_f32_e32 v24, v91, v90
	v_rcp_f32_e32 v41, v41
	v_add_f32_e32 v49, 0x4ce089af, v49
	v_mul_f32_e32 v24, v25, v24
	v_mul_f32_e32 v25, v89, v88
	v_rcp_f32_e32 v49, v49
	v_mul_f32_e32 v25, v32, v25
	v_mul_f32_e32 v32, v87, v86
	v_mul_f32_e32 v32, v33, v32
	v_mul_f32_e32 v33, v85, v84
	v_mul_f32_e32 v33, v41, v33
	v_mul_f32_e32 v41, v83, v82
	v_mul_f32_e32 v41, v49, v41
	v_mul_f32_e32 v49, v81, v80
	v_fmamk_f32 v80, v80, 0xb80b6d22, v206
	v_exp_f32_e32 v80, v80
	v_med3_f32 v16, v16, s1, v207
	v_med3_f32 v17, v17, s1, v207
	v_med3_f32 v24, v24, s1, v207
	v_add_f32_e32 v80, 0x4ce089af, v80
	v_rcp_f32_e32 v80, v80
	v_med3_f32 v25, v25, s1, v207
	v_add_f32_e32 v16, 0x4b400000, v16
	v_add_f32_e32 v17, 0x4b400000, v17
	v_add_f32_e32 v24, 0x4b400000, v24
	v_add_f32_e32 v25, 0x4b400000, v25
	v_mul_f32_e32 v49, v80, v49
	v_perm_b32 v16, v17, v16, s33
	v_perm_b32 v17, v25, v24, s33
	v_perm_b32 v16, v17, v16, s87
	v_med3_f32 v17, v32, s1, v207
	v_med3_f32 v24, v33, s1, v207
	v_med3_f32 v25, v41, s1, v207
	v_med3_f32 v32, v49, s1, v207
	v_add_f32_e32 v17, 0x4b400000, v17
	v_add_f32_e32 v24, 0x4b400000, v24
	v_add_f32_e32 v25, 0x4b400000, v25
	v_add_f32_e32 v32, 0x4b400000, v32
	v_or_b32_e32 v15, 48, v14
	v_perm_b32 v17, v24, v17, s33
	v_perm_b32 v24, v32, v25, s33
	v_perm_b32 v17, v24, v17, s87
	v_mad_i64_i32 v[24:25], s[8:9], v15, s88, v[4:5]
	v_lshl_add_u64 v[24:25], v[24:25], 0, v[2:3]
	global_store_dwordx2 v[24:25], v[16:17], off
	v_fmamk_f32 v17, v78, 0xb80b6d22, v206
	v_exp_f32_e32 v17, v17
	v_fmamk_f32 v24, v76, 0xb80b6d22, v206
	v_exp_f32_e32 v24, v24
	v_fmamk_f32 v25, v74, 0xb80b6d22, v206
	v_exp_f32_e32 v25, v25
	v_fmamk_f32 v32, v72, 0xb80b6d22, v206
	v_exp_f32_e32 v32, v32
	v_fmamk_f32 v33, v70, 0xb80b6d22, v206
	v_add_f32_e32 v17, 0x4ce089af, v17
	v_exp_f32_e32 v33, v33
	v_fmamk_f32 v41, v68, 0xb80b6d22, v206
	v_rcp_f32_e32 v17, v17
	v_add_f32_e32 v24, 0x4ce089af, v24
	v_exp_f32_e32 v41, v41
; __device__ __forceinline__ unsigned cvtpk(float lo, float hi) { unsigned r; asm volatile("v_cvt_pk_bf16_f32 %0, %1, %2" : "=v"(r) : "v"(lo), "v"(hi)); return r; }
;     __device__ __forceinline__ void operator()(const Acc& acc, const Unit& u, int wr, int wc, int fr, int fq) const {
;     ...
;         for (int ai = 0; ai < 2; ++ai)
; #pragma unroll
;             for (int m = 0; m < 4; ++m) { const size_t off = (size_t)(row0 + ai * HALF + m * 16) * ldc + col0;
;                 float h[8];
; #pragma unroll
;                 for (int n = 0; n < 2; ++n)
; #pragma unroll
;                     for (int e = 0; e < 4; ++e) { const float a0 = acc[ai][0][m][n][e], a1 = acc[ai][1][m][n][e];
;                         h[n * 4 + e] = (a0 * a1) * __builtin_amdgcn_rcpf(c3 + __builtin_amdgcn_exp2f(fmaf(a0, c1, c0))); }
;                 if constexpr (FP8OUT == 2) { u32x2 w; w.x = pk4_i8(h[0], h[1], h[2], h[3]); w.y = pk4_i8(h[4], h[5], h[6], h[7]); *(u32x2*)((unsigned char*)H + off) = w; }
;                 else if constexpr (FP8OUT == 1) { u32x2 w; w.x = pk4_fp8_nc(h[0], h[1], h[2], h[3]); w.y = pk4_fp8_nc(h[4], h[5], h[6], h[7]); *(u32x2*)((unsigned char*)H + off) = w; }
;                 else { u32x4 w; w.x = cvtpk(h[0], h[1]); w.y = cvtpk(h[2], h[3]); w.z = cvtpk(h[4], h[5]); w.w = cvtpk(h[6], h[7]); *(u32x4*)((bf16_t*)H + off) = w; } }
	v_fmamk_f32 v49, v66, 0xb80b6d22, v206
	v_rcp_f32_e32 v24, v24
	v_add_f32_e32 v25, 0x4ce089af, v25
	v_exp_f32_e32 v49, v49
	v_rcp_f32_e32 v25, v25
	v_add_f32_e32 v32, 0x4ce089af, v32
	v_mul_f32_e32 v16, v79, v78
	v_rcp_f32_e32 v32, v32
	v_add_f32_e32 v33, 0x4ce089af, v33
	v_mul_f32_e32 v16, v17, v16
	v_mul_f32_e32 v17, v77, v76
	v_rcp_f32_e32 v33, v33
	v_add_f32_e32 v41, 0x4ce089af, v41
	v_mul_f32_e32 v17, v24, v17
	v_mul_f32_e32 v24, v75, v74
	v_rcp_f32_e32 v41, v41
	v_add_f32_e32 v49, 0x4ce089af, v49
	v_mul_f32_e32 v24, v25, v24
	v_mul_f32_e32 v25, v73, v72
	v_rcp_f32_e32 v49, v49
	v_mul_f32_e32 v25, v32, v25
	v_mul_f32_e32 v32, v71, v70
	v_mul_f32_e32 v32, v33, v32
	v_mul_f32_e32 v33, v69, v68
	v_mul_f32_e32 v33, v41, v33
	v_mul_f32_e32 v41, v67, v66
	v_mul_f32_e32 v41, v49, v41
	v_mul_f32_e32 v49, v65, v64
	v_fmamk_f32 v64, v64, 0xb80b6d22, v206
	v_exp_f32_e32 v64, v64
	v_med3_f32 v16, v16, s1, v207
	v_med3_f32 v17, v17, s1, v207
	v_med3_f32 v24, v24, s1, v207
	v_add_f32_e32 v64, 0x4ce089af, v64
	v_rcp_f32_e32 v64, v64
	v_med3_f32 v25, v25, s1, v207
	v_add_f32_e32 v16, 0x4b400000, v16
	v_add_f32_e32 v17, 0x4b400000, v17
	v_add_f32_e32 v24, 0x4b400000, v24
	v_add_f32_e32 v25, 0x4b400000, v25
	v_mul_f32_e32 v49, v64, v49
	v_perm_b32 v16, v17, v16, s33
	v_perm_b32 v17, v25, v24, s33
	v_perm_b32 v16, v17, v16, s87
	v_med3_f32 v17, v32, s1, v207
	v_med3_f32 v24, v33, s1, v207
	v_med3_f32 v25, v41, s1, v207
	v_med3_f32 v32, v49, s1, v207
	v_add_f32_e32 v17, 0x4b400000, v17
	v_add_f32_e32 v24, 0x4b400000, v24
	v_add_f32_e32 v25, 0x4b400000, v25
	v_add_f32_e32 v32, 0x4b400000, v32
	v_add_u32_e32 v15, 0x80, v14
	v_perm_b32 v17, v24, v17, s33
	v_perm_b32 v24, v32, v25, s33
	v_perm_b32 v17, v24, v17, s87
	v_mad_i64_i32 v[24:25], s[8:9], v15, s88, v[4:5]
	v_lshl_add_u64 v[24:25], v[24:25], 0, v[2:3]
	global_store_dwordx2 v[24:25], v[16:17], off
	v_fmamk_f32 v17, v62, 0xb80b6d22, v206
	v_exp_f32_e32 v17, v17
	v_fmamk_f32 v24, v60, 0xb80b6d22, v206
	v_exp_f32_e32 v24, v24
	v_fmamk_f32 v25, v58, 0xb80b6d22, v206
	v_exp_f32_e32 v25, v25
	v_fmamk_f32 v32, v56, 0xb80b6d22, v206
	v_exp_f32_e32 v32, v32
	v_fmamk_f32 v33, v54, 0xb80b6d22, v206
	v_add_f32_e32 v17, 0x4ce089af, v17
	v_exp_f32_e32 v33, v33
	v_fmamk_f32 v41, v52, 0xb80b6d22, v206
	v_rcp_f32_e32 v17, v17
	v_add_f32_e32 v24, 0x4ce089af, v24
	v_exp_f32_e32 v41, v41
	v_fmamk_f32 v49, v50, 0xb80b6d22, v206
	v_mul_f32_e32 v48, v48, v47
	v_fmamk_f32 v47, v47, 0xb80b6d22, v206
	v_rcp_f32_e32 v24, v24
	v_add_f32_e32 v25, 0x4ce089af, v25
	v_exp_f32_e32 v49, v49
	v_exp_f32_e32 v47, v47
	v_rcp_f32_e32 v25, v25
	v_add_f32_e32 v32, 0x4ce089af, v32
	v_mul_f32_e32 v16, v63, v62
	v_rcp_f32_e32 v32, v32
	v_add_f32_e32 v33, 0x4ce089af, v33
	v_mul_f32_e32 v16, v17, v16
	v_mul_f32_e32 v17, v61, v60
	v_rcp_f32_e32 v33, v33
	v_add_f32_e32 v41, 0x4ce089af, v41
	v_mul_f32_e32 v17, v24, v17
	v_mul_f32_e32 v24, v59, v58
	v_rcp_f32_e32 v41, v41
	v_add_f32_e32 v49, 0x4ce089af, v49
	v_add_f32_e32 v47, 0x4ce089af, v47
	v_mul_f32_e32 v24, v25, v24
	v_mul_f32_e32 v25, v57, v56
	v_rcp_f32_e32 v49, v49
	v_rcp_f32_e32 v47, v47
	v_mul_f32_e32 v25, v32, v25
	v_mul_f32_e32 v32, v55, v54
	v_mul_f32_e32 v32, v33, v32
	v_mul_f32_e32 v33, v53, v52
	v_med3_f32 v16, v16, s1, v207
	v_med3_f32 v17, v17, s1, v207
	v_med3_f32 v24, v24, s1, v207
	v_med3_f32 v25, v25, s1, v207
	v_mul_f32_e32 v33, v41, v33
	v_mul_f32_e32 v41, v51, v50
	v_add_f32_e32 v16, 0x4b400000, v16
	v_add_f32_e32 v17, 0x4b400000, v17
	v_add_f32_e32 v24, 0x4b400000, v24
	v_add_f32_e32 v25, 0x4b400000, v25
	v_mul_f32_e32 v41, v49, v41
	v_mul_f32_e32 v47, v47, v48
	v_perm_b32 v16, v17, v16, s33
	v_perm_b32 v17, v25, v24, s33
	v_perm_b32 v16, v17, v16, s87
	v_med3_f32 v17, v32, s1, v207
	v_med3_f32 v24, v33, s1, v207
	v_med3_f32 v25, v41, s1, v207
	v_med3_f32 v32, v47, s1, v207
	v_add_f32_e32 v17, 0x4b400000, v17
	v_add_f32_e32 v24, 0x4b400000, v24
	v_add_f32_e32 v25, 0x4b400000, v25
	v_add_f32_e32 v32, 0x4b400000, v32
	v_add_u32_e32 v15, 0x90, v14
	v_perm_b32 v17, v24, v17, s33
	v_perm_b32 v24, v32, v25, s33
	v_cvt_f32_i32_e32 v40, v40
	v_perm_b32 v17, v24, v17, s87
	v_mad_i64_i32 v[24:25], s[8:9], v15, s88, v[4:5]
	v_lshl_add_u64 v[24:25], v[24:25], 0, v[2:3]
	global_store_dwordx2 v[24:25], v[16:17], off
	v_fmamk_f32 v17, v45, 0xb80b6d22, v206
	v_exp_f32_e32 v17, v17
	v_fmamk_f32 v24, v43, 0xb80b6d22, v206
	v_exp_f32_e32 v24, v24
	v_fmamk_f32 v25, v40, 0xb80b6d22, v206
	v_exp_f32_e32 v25, v25
	v_fmamk_f32 v32, v38, 0xb80b6d22, v206
	v_exp_f32_e32 v32, v32
	v_fmamk_f32 v33, v36, 0xb80b6d22, v206
	v_add_f32_e32 v17, 0x4ce089af, v17
	v_exp_f32_e32 v33, v33
	v_rcp_f32_e32 v17, v17
	v_add_f32_e32 v24, 0x4ce089af, v24
	v_rcp_f32_e32 v24, v24
	v_add_f32_e32 v25, 0x4ce089af, v25
	v_rcp_f32_e32 v25, v25
	v_add_f32_e32 v32, 0x4ce089af, v32
	v_mul_f32_e32 v16, v46, v45
	v_rcp_f32_e32 v32, v32
	v_add_f32_e32 v33, 0x4ce089af, v33
	v_mul_f32_e32 v16, v17, v16
	v_mul_f32_e32 v17, v44, v43
	v_rcp_f32_e32 v33, v33
	v_mul_f32_e32 v17, v24, v17
	v_mul_f32_e32 v24, v42, v40
	v_mul_f32_e32 v24, v25, v24
	v_mul_f32_e32 v25, v39, v38
	v_mul_f32_e32 v25, v32, v25
	v_mul_f32_e32 v32, v37, v36
	v_mul_f32_e32 v32, v33, v32
	v_mul_f32_e32 v33, v35, v34
	v_fmamk_f32 v34, v34, 0xb80b6d22, v206
	v_mul_f32_e32 v31, v31, v30
	v_fmamk_f32 v30, v30, 0xb80b6d22, v206
	v_mul_f32_e32 v29, v29, v28
	v_fmamk_f32 v28, v28, 0xb80b6d22, v206
	v_exp_f32_e32 v34, v34
	v_exp_f32_e32 v30, v30
	v_exp_f32_e32 v28, v28
	v_med3_f32 v16, v16, s1, v207
	v_add_f32_e32 v34, 0x4ce089af, v34
	v_add_f32_e32 v30, 0x4ce089af, v30
	v_add_f32_e32 v28, 0x4ce089af, v28
	v_rcp_f32_e32 v34, v34
	v_rcp_f32_e32 v30, v30
	v_rcp_f32_e32 v28, v28
; __device__ __forceinline__ unsigned cvtpk(float lo, float hi) { unsigned r; asm volatile("v_cvt_pk_bf16_f32 %0, %1, %2" : "=v"(r) : "v"(lo), "v"(hi)); return r; }
;     __device__ __forceinline__ void operator()(const Acc& acc, const Unit& u, int wr, int wc, int fr, int fq) const {
;     ...
;                     for (int e = 0; e < 4; ++e) { const float a0 = acc[ai][0][m][n][e], a1 = acc[ai][1][m][n][e];
;                         h[n * 4 + e] = (a0 * a1) * __builtin_amdgcn_rcpf(c3 + __builtin_amdgcn_exp2f(fmaf(a0, c1, c0))); }
;                 if constexpr (FP8OUT == 2) { u32x2 w; w.x = pk4_i8(h[0], h[1], h[2], h[3]); w.y = pk4_i8(h[4], h[5], h[6], h[7]); *(u32x2*)((unsigned char*)H + off) = w; }
;                 else if constexpr (FP8OUT == 1) { u32x2 w; w.x = pk4_fp8_nc(h[0], h[1], h[2], h[3]); w.y = pk4_fp8_nc(h[4], h[5], h[6], h[7]); *(u32x2*)((unsigned char*)H + off) = w; }
;                 else { u32x4 w; w.x = cvtpk(h[0], h[1]); w.y = cvtpk(h[2], h[3]); w.z = cvtpk(h[4], h[5]); w.w = cvtpk(h[6], h[7]); *(u32x4*)((bf16_t*)H + off) = w; } }
; template <int MODE>
; __device__ __forceinline__ void tr_matrix6(const float* W, int nb, int K, int N, unsigned char* WT, int drows, int rot, int gw, int NGW, int lane, float wscale) {
;     ...
;         for (int j = 0; j < 4; ++j) { float x[32];
; #pragma unroll
;             for (int i = 0; i < 32; ++i) x[i] = v[i][j] * wscale;
;             const v6u w = pk32_fp6(x);
;             *(u32x4*)(dst + (size_t)j * K) = (u32x4){w[0], w[1], w[2], w[3]}; *(u32x4*)(dst + (size_t)j * K + 16) = (u32x4){w[4], w[5], 0u, 0u}; }
	v_med3_f32 v17, v17, s1, v207
	v_med3_f32 v24, v24, s1, v207
	v_med3_f32 v25, v25, s1, v207
	v_add_f32_e32 v16, 0x4b400000, v16
	v_add_f32_e32 v17, 0x4b400000, v17
	v_add_f32_e32 v24, 0x4b400000, v24
	v_add_f32_e32 v25, 0x4b400000, v25
	v_mul_f32_e32 v33, v34, v33
	v_mul_f32_e32 v30, v30, v31
	v_mul_f32_e32 v28, v28, v29
	v_perm_b32 v16, v17, v16, s33
	v_perm_b32 v17, v25, v24, s33
	v_perm_b32 v16, v17, v16, s87
	v_med3_f32 v17, v32, s1, v207
	v_med3_f32 v24, v33, s1, v207
	v_med3_f32 v25, v30, s1, v207
	v_med3_f32 v28, v28, s1, v207
	v_add_f32_e32 v17, 0x4b400000, v17
	v_add_f32_e32 v24, 0x4b400000, v24
	v_add_f32_e32 v25, 0x4b400000, v25
	v_add_f32_e32 v28, 0x4b400000, v28
	v_add_u32_e32 v15, 0xa0, v14
	v_perm_b32 v17, v24, v17, s33
	v_perm_b32 v24, v28, v25, s33
	v_perm_b32 v17, v24, v17, s87
	v_mad_i64_i32 v[24:25], s[8:9], v15, s88, v[4:5]
	v_lshl_add_u64 v[24:25], v[24:25], 0, v[2:3]
	global_store_dwordx2 v[24:25], v[16:17], off
	v_fmamk_f32 v16, v26, 0xb80b6d22, v206
	v_exp_f32_e32 v16, v16
	v_fmamk_f32 v17, v22, 0xb80b6d22, v206
	v_exp_f32_e32 v17, v17
	v_mul_f32_e32 v15, v27, v26
	v_add_f32_e32 v16, 0x4ce089af, v16
	v_rcp_f32_e32 v16, v16
	v_add_f32_e32 v17, 0x4ce089af, v17
	v_rcp_f32_e32 v17, v17
	v_mul_f32_e32 v19, v19, v18
	v_mul_f32_e32 v15, v16, v15
	v_mul_f32_e32 v16, v23, v22
	v_mul_f32_e32 v16, v17, v16
	v_mul_f32_e32 v17, v21, v20
	v_fmamk_f32 v20, v20, 0xb80b6d22, v206
	v_fmamk_f32 v18, v18, 0xb80b6d22, v206
	v_exp_f32_e32 v20, v20
	v_exp_f32_e32 v18, v18
	v_mul_f32_e32 v13, v13, v12
	v_fmamk_f32 v12, v12, 0xb80b6d22, v206
	v_mul_f32_e32 v11, v11, v10
	v_fmamk_f32 v10, v10, 0xb80b6d22, v206
	v_mul_f32_e32 v9, v9, v8
	v_fmamk_f32 v8, v8, 0xb80b6d22, v206
	v_mul_f32_e32 v7, v7, v6
	v_fmamk_f32 v6, v6, 0xb80b6d22, v206
	v_exp_f32_e32 v12, v12
	v_exp_f32_e32 v10, v10
	v_exp_f32_e32 v8, v8
	v_exp_f32_e32 v6, v6
	v_add_f32_e32 v20, 0x4ce089af, v20
	v_add_f32_e32 v18, 0x4ce089af, v18
	v_rcp_f32_e32 v20, v20
	v_rcp_f32_e32 v18, v18
	v_add_f32_e32 v12, 0x4ce089af, v12
	v_add_f32_e32 v10, 0x4ce089af, v10
	v_add_f32_e32 v8, 0x4ce089af, v8
	v_add_f32_e32 v6, 0x4ce089af, v6
	v_rcp_f32_e32 v12, v12
	v_rcp_f32_e32 v10, v10
	v_rcp_f32_e32 v8, v8
	v_rcp_f32_e32 v6, v6
	v_mul_f32_e32 v17, v20, v17
	v_mul_f32_e32 v18, v18, v19
	v_mul_f32_e32 v12, v12, v13
	v_mul_f32_e32 v10, v10, v11
	v_mul_f32_e32 v8, v8, v9
	v_mul_f32_e32 v7, v6, v7
	v_med3_f32 v6, v15, s1, v207
	v_med3_f32 v9, v16, s1, v207
	v_med3_f32 v11, v17, s1, v207
	v_med3_f32 v13, v18, s1, v207
	v_add_f32_e32 v6, 0x4b400000, v6
	v_add_f32_e32 v9, 0x4b400000, v9
	v_add_f32_e32 v11, 0x4b400000, v11
	v_add_f32_e32 v13, 0x4b400000, v13
	v_perm_b32 v6, v9, v6, s33
	v_perm_b32 v9, v13, v11, s33
	v_perm_b32 v6, v9, v6, s87
	v_med3_f32 v9, v12, s1, v207
	v_med3_f32 v10, v10, s1, v207
	v_med3_f32 v8, v8, s1, v207
	v_med3_f32 v7, v7, s1, v207
	v_add_u32_e32 v14, 0xb0, v14
	v_add_f32_e32 v9, 0x4b400000, v9
	v_add_f32_e32 v10, 0x4b400000, v10
	v_add_f32_e32 v8, 0x4b400000, v8
	v_add_f32_e32 v7, 0x4b400000, v7
	v_perm_b32 v9, v10, v9, s33
	v_perm_b32 v7, v7, v8, s33
	v_mad_i64_i32 v[4:5], s[8:9], v14, s88, v[4:5]
	v_perm_b32 v7, v7, v9, s87
	v_lshl_add_u64 v[2:3], v[4:5], 0, v[2:3]
	s_cmp_lt_u32 s98, 14
	s_cbranch_scc0 .Lp8f_e
	s_waitcnt vmcnt(7)
	v_mul_f32_e32 v208, 0x42b40000, v208
	v_mul_f32_e32 v209, 0x42b40000, v209
	v_mul_f32_e32 v210, 0x42b40000, v210
	v_mul_f32_e32 v211, 0x42b40000, v211
	v_mul_f32_e32 v212, 0x42b40000, v212
	v_mul_f32_e32 v213, 0x42b40000, v213
	v_mul_f32_e32 v214, 0x42b40000, v214
	v_mul_f32_e32 v215, 0x42b40000, v215
	v_mul_f32_e32 v216, 0x42b40000, v216
	v_mul_f32_e32 v217, 0x42b40000, v217
	v_mul_f32_e32 v218, 0x42b40000, v218
	v_mul_f32_e32 v219, 0x42b40000, v219
	v_mul_f32_e32 v220, 0x42b40000, v220
	v_mul_f32_e32 v221, 0x42b40000, v221
	v_mul_f32_e32 v222, 0x42b40000, v222
	v_mul_f32_e32 v223, 0x42b40000, v223
	v_mul_f32_e32 v224, 0x42b40000, v224
	v_mul_f32_e32 v225, 0x42b40000, v225
	v_mul_f32_e32 v226, 0x42b40000, v226
	v_mul_f32_e32 v227, 0x42b40000, v227
	v_mul_f32_e32 v228, 0x42b40000, v228
	v_mul_f32_e32 v229, 0x42b40000, v229
	v_mul_f32_e32 v230, 0x42b40000, v230
	v_mul_f32_e32 v231, 0x42b40000, v231
	v_mul_f32_e32 v232, 0x42b40000, v232
	v_mul_f32_e32 v233, 0x42b40000, v233
	v_mul_f32_e32 v234, 0x42b40000, v234
	v_mul_f32_e32 v235, 0x42b40000, v235
	v_mul_f32_e32 v236, 0x42b40000, v236
	v_mul_f32_e32 v237, 0x42b40000, v237
	v_mul_f32_e32 v238, 0x42b40000, v238
	v_mul_f32_e32 v239, 0x42b40000, v239
	v_med3_f32 v208, v208, v255, v254
	v_med3_f32 v209, v209, v255, v254
	v_med3_f32 v210, v210, v255, v254
	v_med3_f32 v211, v211, v255, v254
	v_med3_f32 v212, v212, v255, v254
	v_med3_f32 v213, v213, v255, v254
	v_med3_f32 v214, v214, v255, v254
	v_med3_f32 v215, v215, v255, v254
	v_med3_f32 v216, v216, v255, v254
	v_med3_f32 v217, v217, v255, v254
	v_med3_f32 v218, v218, v255, v254
	v_med3_f32 v219, v219, v255, v254
	v_med3_f32 v220, v220, v255, v254
	v_med3_f32 v221, v221, v255, v254
	v_med3_f32 v222, v222, v255, v254
	v_med3_f32 v223, v223, v255, v254
	v_med3_f32 v224, v224, v255, v254
	v_med3_f32 v225, v225, v255, v254
	v_med3_f32 v226, v226, v255, v254
	v_med3_f32 v227, v227, v255, v254
	v_med3_f32 v228, v228, v255, v254
	v_med3_f32 v229, v229, v255, v254
	v_med3_f32 v230, v230, v255, v254
	v_med3_f32 v231, v231, v255, v254
	v_med3_f32 v232, v232, v255, v254
	v_med3_f32 v233, v233, v255, v254
	v_med3_f32 v234, v234, v255, v254
	v_med3_f32 v235, v235, v255, v254
	v_med3_f32 v236, v236, v255, v254
	v_med3_f32 v237, v237, v255, v254
	v_med3_f32 v238, v238, v255, v254
	v_med3_f32 v239, v239, v255, v254
	v_cvt_scalef32_2xpk16_fp6_f32 v[240:245], v[208:223], v[224:239], 1.0
	v_readlane_b32 s100, v252, 6
	v_readlane_b32 s101, v252, 7
	s_lshr_b32 s99, s98, 1
	s_lshl_b32 s99, s99, 19
	s_add_u32 s100, s100, s99
	s_addc_u32 s101, s101, 0
	s_and_b32 s99, s98, 1
	s_lshl_b32 s99, s99, 17
	s_add_u32 s100, s100, s99
	s_addc_u32 s101, s101, 0
	global_store_dwordx4 v249, v[240:243], s[100:101]
	global_store_dwordx4 v249, v[244:247], s[100:101] offset:16
	s_add_i32 s98, s98, 1

; template <int MODE>
; __device__ __forceinline__ void tr_matrix6(const float* W, int nb, int K, int N, unsigned char* WT, int drows, int rot, int gw, int NGW, int lane, float wscale) {
;     ...
;     const int c = lane & 7, q = lane >> 3;
;     for (; it < total; it += NGW) {
;         const int e = it / per, r = it - e * per, kb = r / nbn, nbk = r - kb * nbn, n0 = nbk * 32, k0 = kb * 256;
;         const float* src = W + (size_t)e * K * N + (size_t)(k0 + 32 * q) * N + n0 + 4 * c;
;         f32x4 v[32];
; #pragma unroll
;         for (int i = 0; i < 32; ++i) v[i] = *(const f32x4*)(src + (size_t)i * N);
;         const int drow0 = (MODE == 0) ? n0 : ((n0 >> 7) * 256 + (n0 & 127) + (MODE == 2 ? 128 : 0));
;         unsigned char* dst = WT + (size_t)e * drows * K + (size_t)(drow0 + 4 * c) * K + k0 + 32 * q;
; #pragma unroll
;         for (int j = 0; j < 4; ++j) { float x[32];
; #pragma unroll
;             for (int i = 0; i < 32; ++i) x[i] = v[i][j] * wscale;
;             const v6u w = pk32_fp6(x);
;             *(u32x4*)(dst + (size_t)j * K) = (u32x4){w[0], w[1], w[2], w[3]}; *(u32x4*)(dst + (size_t)j * K + 16) = (u32x4){w[4], w[5], 0u, 0u}; }
.LBB0_601:
.Lp8f_fb:
	s_cmp_lt_u32 s98, 14
	s_cbranch_scc0 .Lp8f_fbd
	v_readlane_b32 s100, v252, 4
	v_readlane_b32 s101, v252, 5
	s_lshl_b32 s99, s98, 8
	s_nop 1
	s_add_u32 s100, s100, s99
	s_addc_u32 s101, s101, 0
	global_load_dword v208, v248, s[100:101]
	s_add_u32 s100, s100, 0x7000
	s_addc_u32 s101, s101, 0
	global_load_dword v209, v248, s[100:101]
	s_add_u32 s100, s100, 0x7000
	s_addc_u32 s101, s101, 0
	global_load_dword v210, v248, s[100:101]
	s_add_u32 s100, s100, 0x7000
	s_addc_u32 s101, s101, 0
	global_load_dword v211, v248, s[100:101]
	s_add_u32 s100, s100, 0x7000
	s_addc_u32 s101, s101, 0
	global_load_dword v212, v248, s[100:101]
	s_add_u32 s100, s100, 0x7000
	s_addc_u32 s101, s101, 0
	global_load_dword v213, v248, s[100:101]
	s_add_u32 s100, s100, 0x7000
	s_addc_u32 s101, s101, 0
	global_load_dword v214, v248, s[100:101]
	s_add_u32 s100, s100, 0x7000
	s_addc_u32 s101, s101, 0
	global_load_dword v215, v248, s[100:101]
	s_add_u32 s100, s100, 0x7000
	s_addc_u32 s101, s101, 0
	global_load_dword v216, v248, s[100:101]
	s_add_u32 s100, s100, 0x7000
	s_addc_u32 s101, s101, 0
	global_load_dword v217, v248, s[100:101]
	s_add_u32 s100, s100, 0x7000
	s_addc_u32 s101, s101, 0
	global_load_dword v218, v248, s[100:101]
	s_add_u32 s100, s100, 0x7000
	s_addc_u32 s101, s101, 0
	global_load_dword v219, v248, s[100:101]
	s_add_u32 s100, s100, 0x7000
	s_addc_u32 s101, s101, 0
	global_load_dword v220, v248, s[100:101]
	s_add_u32 s100, s100, 0x7000
	s_addc_u32 s101, s101, 0
	global_load_dword v221, v248, s[100:101]
	s_add_u32 s100, s100, 0x7000
	s_addc_u32 s101, s101, 0
	global_load_dword v222, v248, s[100:101]
	s_add_u32 s100, s100, 0x7000
	s_addc_u32 s101, s101, 0
	global_load_dword v223, v248, s[100:101]
	s_add_u32 s100, s100, 0x7000
	s_addc_u32 s101, s101, 0
	global_load_dword v224, v248, s[100:101]
	s_add_u32 s100, s100, 0x7000
	s_addc_u32 s101, s101, 0
	global_load_dword v225, v248, s[100:101]
	s_add_u32 s100, s100, 0x7000
	s_addc_u32 s101, s101, 0
	global_load_dword v226, v248, s[100:101]
	s_add_u32 s100, s100, 0x7000
	s_addc_u32 s101, s101, 0
	global_load_dword v227, v248, s[100:101]
	s_add_u32 s100, s100, 0x7000
	s_addc_u32 s101, s101, 0
	global_load_dword v228, v248, s[100:101]
	s_add_u32 s100, s100, 0x7000
	s_addc_u32 s101, s101, 0
	global_load_dword v229, v248, s[100:101]
	s_add_u32 s100, s100, 0x7000
	s_addc_u32 s101, s101, 0
	global_load_dword v230, v248, s[100:101]
	s_add_u32 s100, s100, 0x7000
	s_addc_u32 s101, s101, 0
	global_load_dword v231, v248, s[100:101]
	s_add_u32 s100, s100, 0x7000
	s_addc_u32 s101, s101, 0
	global_load_dword v232, v248, s[100:101]
	s_add_u32 s100, s100, 0x7000
	s_addc_u32 s101, s101, 0
	global_load_dword v233, v248, s[100:101]
	s_add_u32 s100, s100, 0x7000
	s_addc_u32 s101, s101, 0
	global_load_dword v234, v248, s[100:101]
	s_add_u32 s100, s100, 0x7000
	s_addc_u32 s101, s101, 0
	global_load_dword v235, v248, s[100:101]
	s_add_u32 s100, s100, 0x7000
	s_addc_u32 s101, s101, 0
	global_load_dword v236, v248, s[100:101]
	s_add_u32 s100, s100, 0x7000
	s_addc_u32 s101, s101, 0
	global_load_dword v237, v248, s[100:101]
	s_add_u32 s100, s100, 0x7000
	s_addc_u32 s101, s101, 0
	global_load_dword v238, v248, s[100:101]
	s_add_u32 s100, s100, 0x7000
	s_addc_u32 s101, s101, 0
	global_load_dword v239, v248, s[100:101]
	s_waitcnt vmcnt(0)
	v_mul_f32_e32 v208, 0x42b40000, v208
	v_mul_f32_e32 v209, 0x42b40000, v209
	v_mul_f32_e32 v210, 0x42b40000, v210
	v_mul_f32_e32 v211, 0x42b40000, v211
	v_mul_f32_e32 v212, 0x42b40000, v212
	v_mul_f32_e32 v213, 0x42b40000, v213
	v_mul_f32_e32 v214, 0x42b40000, v214
	v_mul_f32_e32 v215, 0x42b40000, v215
	v_mul_f32_e32 v216, 0x42b40000, v216
	v_mul_f32_e32 v217, 0x42b40000, v217
	v_mul_f32_e32 v218, 0x42b40000, v218
	v_mul_f32_e32 v219, 0x42b40000, v219
	v_mul_f32_e32 v220, 0x42b40000, v220
	v_mul_f32_e32 v221, 0x42b40000, v221
	v_mul_f32_e32 v222, 0x42b40000, v222
	v_mul_f32_e32 v223, 0x42b40000, v223
	v_mul_f32_e32 v224, 0x42b40000, v224
	v_mul_f32_e32 v225, 0x42b40000, v225
	v_mul_f32_e32 v226, 0x42b40000, v226
	v_mul_f32_e32 v227, 0x42b40000, v227
	v_mul_f32_e32 v228, 0x42b40000, v228
	v_mul_f32_e32 v229, 0x42b40000, v229
	v_mul_f32_e32 v230, 0x42b40000, v230
	v_mul_f32_e32 v231, 0x42b40000, v231
	v_mul_f32_e32 v232, 0x42b40000, v232
	v_mul_f32_e32 v233, 0x42b40000, v233
	v_mul_f32_e32 v234, 0x42b40000, v234
	v_mul_f32_e32 v235, 0x42b40000, v235
	v_mul_f32_e32 v236, 0x42b40000, v236
	v_mul_f32_e32 v237, 0x42b40000, v237
	v_mul_f32_e32 v238, 0x42b40000, v238
	v_mul_f32_e32 v239, 0x42b40000, v239
	v_med3_f32 v208, v208, v255, v254
	v_med3_f32 v209, v209, v255, v254
	v_med3_f32 v210, v210, v255, v254
	v_med3_f32 v211, v211, v255, v254
	v_med3_f32 v212, v212, v255, v254
	v_med3_f32 v213, v213, v255, v254
	v_med3_f32 v214, v214, v255, v254
	v_med3_f32 v215, v215, v255, v254
	v_med3_f32 v216, v216, v255, v254
	v_med3_f32 v217, v217, v255, v254
	v_med3_f32 v218, v218, v255, v254
	v_med3_f32 v219, v219, v255, v254
	v_med3_f32 v220, v220, v255, v254
	v_med3_f32 v221, v221, v255, v254
	v_med3_f32 v222, v222, v255, v254
	v_med3_f32 v223, v223, v255, v254
	v_med3_f32 v224, v224, v255, v254
	v_med3_f32 v225, v225, v255, v254
	v_med3_f32 v226, v226, v255, v254
	v_med3_f32 v227, v227, v255, v254
	v_med3_f32 v228, v228, v255, v254
	v_med3_f32 v229, v229, v255, v254
	v_med3_f32 v230, v230, v255, v254
	v_med3_f32 v231, v231, v255, v254
	v_med3_f32 v232, v232, v255, v254
	v_med3_f32 v233, v233, v255, v254
	v_med3_f32 v234, v234, v255, v254
	v_med3_f32 v235, v235, v255, v254
	v_med3_f32 v236, v236, v255, v254
	v_med3_f32 v237, v237, v255, v254
	v_med3_f32 v238, v238, v255, v254
	v_med3_f32 v239, v239, v255, v254
	v_cvt_scalef32_2xpk16_fp6_f32 v[240:245], v[208:223], v[224:239], 1.0
	v_readlane_b32 s100, v252, 6
	v_readlane_b32 s101, v252, 7
	s_lshr_b32 s99, s98, 1
	s_lshl_b32 s99, s99, 19
	s_add_u32 s100, s100, s99
	s_addc_u32 s101, s101, 0
	s_and_b32 s99, s98, 1
	s_lshl_b32 s99, s99, 17
	s_add_u32 s100, s100, s99
	s_addc_u32 s101, s101, 0
	global_store_dwordx4 v249, v[240:243], s[100:101]
	global_store_dwordx4 v249, v[244:247], s[100:101] offset:16
	s_add_i32 s98, s98, 1
	s_branch .Lp8f_fb
